# topk min/max sort networks + peer_gather: VOP3P int4 dots without zero-init movs, weight broadcast via one f16 convert + readlane SGPR operand
# speedup vs baseline: 1.0111x; 1.0009x over previous
.LBB0_763:
	s_cmpk_eq_i32 s58, 0x80
	s_cselect_b64 s[12:13], -1, 0
	ds_bpermute_b32 v84, v93, v92
	s_and_b64 vcc, s[12:13], s[48:49]
	v_cndmask_b32_e32 v104, v0, v94, vcc
	v_ashrrev_i32_e32 v105, 31, v104
	s_and_b32 s12, s58, 0x70
	v_lshlrev_b64 v[104:105], 9, v[104:105]
	v_lshl_add_u64 v[104:105], s[94:95], 0, v[104:105]
	s_lshl_b32 s36, s12, 2
	s_waitcnt lgkmcnt(0)
	v_ashrrev_i32_e32 v85, 31, v84
	v_lshl_add_u64 v[104:105], v[104:105], 0, s[36:37]
	v_lshl_add_u64 v[84:85], v[84:85], 3, s[8:9]
	v_lshl_add_u64 v[104:105], v[104:105], 0, v[144:145]
	global_load_dwordx2 v[84:85], v[84:85], off
	s_nop 0
	global_load_dword v86, v[72:73], off
	global_load_dword v92, v[104:105], off
	s_waitcnt vmcnt(11)
	v_dot8_i32_i4 v87, v8, v1, 0
	v_dot8_i32_i4 v104, v8, v88, 0
	v_dot8_i32_i4 v87, v9, v89, v87
	v_dot8_i32_i4 v104, v9, v90, v104
	s_waitcnt vmcnt(10)
	v_dot8_i32_i4 v9, v10, v88, 0
	v_dot8_i32_i4 v9, v11, v90, v9
	v_lshl_add_u32 v8, v87, 4, v104
	v_cvt_f32_i32_e32 v87, v8
	v_dot8_i32_i4 v8, v10, v1, 0
	v_dot8_i32_i4 v8, v11, v89, v8
	s_add_i32 s58, s58, 16
	v_lshl_add_u64 v[72:73], v[72:73], 0, 64
	s_waitcnt vmcnt(2)
	v_mul_f32_e32 v85, v91, v85
	v_lshl_add_u32 v8, v8, 4, v9
	v_cvt_f32_i32_e32 v104, v8
	v_dot8_i32_i4 v8, v12, v1, 0
	v_dot8_i32_i4 v9, v12, v88, 0
	v_dot8_i32_i4 v8, v13, v89, v8
	v_dot8_i32_i4 v9, v13, v90, v9
	s_waitcnt vmcnt(0)
	v_readlane_b32 s12, v92, 0
	v_readlane_b32 s28, v92, 8
	v_readlane_b32 s30, v92, 9
	v_lshl_add_u32 v8, v8, 4, v9
	v_cvt_f32_i32_e32 v105, v8
	v_dot8_i32_i4 v8, v14, v1, 0
	v_dot8_i32_i4 v9, v14, v88, 0
	v_dot8_i32_i4 v8, v15, v89, v8
	v_dot8_i32_i4 v9, v15, v90, v9
	s_ashr_i32 s13, s12, 31
	v_readlane_b32 s14, v92, 1
	s_ashr_i32 s29, s28, 31
	v_lshl_add_u32 v8, v8, 4, v9
	v_cvt_f32_i32_e32 v106, v8
	v_dot8_i32_i4 v8, v16, v1, 0
	v_dot8_i32_i4 v9, v16, v88, 0
	v_dot8_i32_i4 v8, v17, v89, v8
	v_dot8_i32_i4 v9, v17, v90, v9
	s_ashr_i32 s31, s30, 31
	v_readlane_b32 s34, v92, 10
	s_lshl_b64 s[12:13], s[12:13], 9
	v_lshl_add_u32 v8, v8, 4, v9
	v_cvt_f32_i32_e32 v107, v8
	v_dot8_i32_i4 v8, v18, v1, 0
	v_dot8_i32_i4 v9, v18, v88, 0
	v_dot8_i32_i4 v8, v19, v89, v8
	v_dot8_i32_i4 v9, v19, v90, v9
	s_ashr_i32 s15, s14, 31
	v_readlane_b32 s16, v92, 2
	s_lshl_b64 s[28:29], s[28:29], 9
	v_lshl_add_u32 v8, v8, 4, v9
	v_cvt_f32_i32_e32 v108, v8
	v_dot8_i32_i4 v8, v20, v1, 0
	v_dot8_i32_i4 v9, v20, v88, 0
	v_dot8_i32_i4 v8, v21, v89, v8
	v_dot8_i32_i4 v9, v21, v90, v9
	s_lshl_b64 s[30:31], s[30:31], 9
	s_ashr_i32 s35, s34, 31
	v_readlane_b32 s38, v92, 11
	v_lshl_add_u32 v8, v8, 4, v9
	v_cvt_f32_i32_e32 v109, v8
	v_dot8_i32_i4 v8, v22, v1, 0
	v_dot8_i32_i4 v9, v22, v88, 0
	v_dot8_i32_i4 v8, v23, v89, v8
	v_dot8_i32_i4 v9, v23, v90, v9
	s_lshl_b64 s[14:15], s[14:15], 9
	s_ashr_i32 s17, s16, 31
	v_readlane_b32 s18, v92, 3
	v_lshl_add_u32 v8, v8, 4, v9
	v_cvt_f32_i32_e32 v110, v8
	v_dot8_i32_i4 v8, v24, v1, 0
	v_dot8_i32_i4 v9, v24, v88, 0
	v_dot8_i32_i4 v8, v25, v89, v8
	v_dot8_i32_i4 v9, v25, v90, v9
	v_lshl_add_u64 v[24:25], v[4:5], 0, s[28:29]
	s_lshl_b64 s[34:35], s[34:35], 9
	s_ashr_i32 s39, s38, 31
	v_lshl_add_u32 v8, v8, 4, v9
	v_cvt_f32_i32_e32 v111, v8
	v_dot8_i32_i4 v8, v38, v1, 0
	v_dot8_i32_i4 v9, v38, v88, 0
	v_dot8_i32_i4 v8, v39, v89, v8
	v_dot8_i32_i4 v9, v39, v90, v9
	v_cndmask_b32_e64 v119, v87, v111, s[40:41]
	v_cndmask_b32_e64 v87, v111, v87, s[40:41]
	ds_bpermute_b32 v111, v184, v119
	v_lshl_add_u32 v8, v8, 4, v9
	v_cvt_f32_i32_e32 v112, v8
	v_dot8_i32_i4 v8, v50, v1, 0
	v_dot8_i32_i4 v9, v50, v88, 0
	v_dot8_i32_i4 v8, v51, v89, v8
	v_dot8_i32_i4 v9, v51, v90, v9
	s_waitcnt lgkmcnt(0)
	v_add_f32_e32 v87, v87, v111
	v_cndmask_b32_e64 v111, v104, v112, s[40:41]
	ds_bpermute_b32 v111, v184, v111
	v_lshl_add_u32 v8, v8, 4, v9
	v_cvt_f32_i32_e32 v113, v8
	v_dot8_i32_i4 v8, v48, v1, 0
	v_dot8_i32_i4 v9, v48, v88, 0
	v_cndmask_b32_e64 v104, v112, v104, s[40:41]
	v_dot8_i32_i4 v8, v49, v89, v8
	v_dot8_i32_i4 v9, v49, v90, v9
	s_waitcnt lgkmcnt(0)
	v_add_f32_e32 v104, v104, v111
	v_cndmask_b32_e64 v111, v105, v113, s[40:41]
	ds_bpermute_b32 v111, v184, v111
	v_lshl_add_u32 v8, v8, 4, v9
	v_cvt_f32_i32_e32 v114, v8
	v_dot8_i32_i4 v8, v46, v1, 0
	v_dot8_i32_i4 v9, v46, v88, 0
	v_cndmask_b32_e64 v105, v113, v105, s[40:41]
	v_dot8_i32_i4 v8, v47, v89, v8
	v_dot8_i32_i4 v9, v47, v90, v9
	s_waitcnt lgkmcnt(0)
	v_add_f32_e32 v105, v105, v111
	v_cndmask_b32_e64 v111, v106, v114, s[40:41]
	ds_bpermute_b32 v111, v184, v111
	v_lshl_add_u32 v8, v8, 4, v9
	v_cvt_f32_i32_e32 v115, v8
	v_dot8_i32_i4 v8, v44, v1, 0
	v_dot8_i32_i4 v9, v44, v88, 0
	v_cndmask_b32_e64 v106, v114, v106, s[40:41]
	v_dot8_i32_i4 v8, v45, v89, v8
	v_dot8_i32_i4 v9, v45, v90, v9
	s_waitcnt lgkmcnt(0)
	v_add_f32_e32 v106, v106, v111
	v_cndmask_b32_e64 v111, v107, v115, s[40:41]
	ds_bpermute_b32 v111, v184, v111
	v_lshl_add_u32 v8, v8, 4, v9
	v_cvt_f32_i32_e32 v116, v8
	v_dot8_i32_i4 v8, v42, v1, 0
	v_dot8_i32_i4 v9, v42, v88, 0
	v_cndmask_b32_e64 v107, v115, v107, s[40:41]
	v_dot8_i32_i4 v8, v43, v89, v8
	v_dot8_i32_i4 v9, v43, v90, v9
	s_waitcnt lgkmcnt(0)
	v_add_f32_e32 v107, v107, v111
	v_cndmask_b32_e64 v111, v108, v116, s[40:41]
	ds_bpermute_b32 v111, v184, v111
	v_lshl_add_u32 v8, v8, 4, v9
	v_cvt_f32_i32_e32 v117, v8
	v_dot8_i32_i4 v8, v40, v1, 0
	v_dot8_i32_i4 v9, v40, v88, 0
	v_cndmask_b32_e64 v108, v116, v108, s[40:41]
	v_dot8_i32_i4 v8, v41, v89, v8
	v_dot8_i32_i4 v9, v41, v90, v9
	s_waitcnt lgkmcnt(0)
	v_add_f32_e32 v108, v108, v111
	v_cndmask_b32_e64 v111, v109, v117, s[40:41]
	ds_bpermute_b32 v111, v184, v111
	v_lshl_add_u32 v8, v8, 4, v9
	v_cvt_f32_i32_e32 v118, v8
	v_cndmask_b32_e64 v109, v117, v109, s[40:41]
	v_lshl_add_u64 v[38:39], v[4:5], 0, s[30:31]
	s_waitcnt lgkmcnt(0)
	v_add_f32_e32 v109, v109, v111
	v_cndmask_b32_e64 v111, v110, v118, s[40:41]
	ds_bpermute_b32 v111, v184, v111
	v_cndmask_b32_e64 v110, v118, v110, s[40:41]
	v_readlane_b32 s50, v92, 12
	s_lshl_b64 s[16:17], s[16:17], 9
	s_ashr_i32 s19, s18, 31
	s_waitcnt lgkmcnt(0)
	v_add_f32_e32 v110, v110, v111
	v_cndmask_b32_e64 v111, v87, v107, s[42:43]
	v_cndmask_b32_e64 v87, v107, v87, s[42:43]
	ds_bpermute_b32 v107, v185, v111
	v_readlane_b32 s20, v92, 4
	global_load_dwordx2 v[24:25], v[24:25], off
	v_lshl_add_u64 v[40:41], v[4:5], 0, s[34:35]
	global_load_dwordx2 v[38:39], v[38:39], off
	s_waitcnt lgkmcnt(0)
	v_add_f32_e32 v87, v87, v107
	v_cndmask_b32_e64 v107, v104, v108, s[42:43]
	ds_bpermute_b32 v107, v185, v107
	v_cndmask_b32_e64 v104, v108, v104, s[42:43]
	s_lshl_b64 s[38:39], s[38:39], 9
	s_ashr_i32 s51, s50, 31
	v_readlane_b32 s52, v92, 13
	s_waitcnt lgkmcnt(0)
	v_add_f32_e32 v104, v104, v107
	v_cndmask_b32_e64 v107, v105, v109, s[42:43]
	ds_bpermute_b32 v107, v185, v107
	v_cndmask_b32_e64 v105, v109, v105, s[42:43]
	s_lshl_b64 s[18:19], s[18:19], 9
	s_ashr_i32 s21, s20, 31
	v_readlane_b32 s22, v92, 5
	s_waitcnt lgkmcnt(0)
	v_add_f32_e32 v105, v105, v107
	v_cndmask_b32_e64 v107, v106, v110, s[42:43]
	ds_bpermute_b32 v107, v185, v107
	v_cndmask_b32_e64 v106, v110, v106, s[42:43]
	global_load_dwordx2 v[50:51], v[40:41], off
	s_lshl_b64 s[50:51], s[50:51], 9
	s_ashr_i32 s53, s52, 31
	s_waitcnt lgkmcnt(0)
	v_add_f32_e32 v106, v106, v107
	v_cndmask_b32_e64 v107, v87, v105, s[44:45]
	v_cndmask_b32_e64 v87, v105, v87, s[44:45]
	ds_bpermute_b32 v105, v186, v107
	v_readlane_b32 s54, v92, 14
	s_lshl_b64 s[20:21], s[20:21], 9
	s_ashr_i32 s23, s22, 31
	v_readlane_b32 s24, v92, 6
	s_waitcnt lgkmcnt(0)
	v_add_f32_e32 v87, v87, v105
	v_cndmask_b32_e64 v105, v104, v106, s[44:45]
	ds_bpermute_b32 v105, v186, v105
	v_cndmask_b32_e64 v104, v106, v104, s[44:45]
	s_lshl_b64 s[52:53], s[52:53], 9
	s_ashr_i32 s55, s54, 31
	v_readlane_b32 s56, v92, 15
	s_waitcnt lgkmcnt(0)
	v_add_f32_e32 v104, v104, v105
	v_cndmask_b32_e64 v105, v87, v104, s[46:47]
	v_cndmask_b32_e64 v87, v104, v87, s[46:47]
	ds_bpermute_b32 v104, v187, v105
	s_lshl_b64 s[22:23], s[22:23], 9
	s_ashr_i32 s25, s24, 31
	v_readlane_b32 s26, v92, 7
	s_lshl_b64 s[54:55], s[54:55], 9
	s_waitcnt lgkmcnt(0)
	v_add_f32_e32 v87, v87, v104
	ds_bpermute_b32 v104, v188, v87
	s_ashr_i32 s57, s56, 31
	s_lshl_b64 s[24:25], s[24:25], 9
	s_ashr_i32 s27, s26, 31
	s_lshl_b64 s[56:57], s[56:57], 9
	s_waitcnt lgkmcnt(0)
	v_add_f32_e32 v87, v87, v104
	ds_bpermute_b32 v104, v189, v87
	s_lshl_b64 s[26:27], s[26:27], 9
	v_lshl_add_u64 v[8:9], v[4:5], 0, s[12:13]
	v_lshl_add_u64 v[10:11], v[4:5], 0, s[14:15]
	v_lshl_add_u64 v[12:13], v[4:5], 0, s[16:17]
	s_waitcnt lgkmcnt(0)
	v_add_f32_e32 v87, v87, v104
	v_add_f32_e32 v87, v95, v87
	v_mul_f32_e32 v85, v85, v87
	v_mul_f32_e32 v87, 0x3d372713, v85
	v_mul_f32_e32 v87, v85, v87
	v_fma_f32 v87, v85, v87, v85
	v_mul_f32_e32 v87, 0x3fcc422a, v87
	v_mul_f32_e32 v87, 0xbfb8aa3b, v87
	v_exp_f32_e32 v87, v87
	v_lshlrev_b32_e32 v104, 4, v82
	v_lshl_add_u64 v[14:15], v[4:5], 0, s[18:19]
	v_lshl_add_u64 v[16:17], v[4:5], 0, s[20:21]
	v_add_f32_e32 v87, 1.0, v87
	v_rcp_f32_e32 v87, v87
	v_lshl_add_u64 v[18:19], v[4:5], 0, s[22:23]
	v_lshl_add_u64 v[20:21], v[4:5], 0, s[24:25]
	v_lshl_add_u64 v[22:23], v[4:5], 0, s[26:27]
	v_pk_mul_f32 v[84:85], v[84:85], v[86:87]
	v_lshrrev_b32_e32 v87, 4, v82
	v_pk_mul_f32 v[84:85], v[84:85], v[84:85] op_sel:[0,1] op_sel_hi:[1,0]
	v_cvt_f16_f32_e32 v120, v84
	v_and_b32_e32 v86, 0x7070707, v82
	v_readlane_b32 s36, v120, 0
	v_and_b32_e32 v87, 0x7070707, v87
	v_perm_b32 v86, s2, v205, v86
	v_perm_b32 v87, s2, v205, v87
	v_and_or_b32 v86, v104, s4, v86
	v_and_or_b32 v82, v82, s4, v87
	v_perm_b32 v87, v82, v86, s5
	v_perm_b32 v104, v82, v86, s33
	v_perm_b32 v105, v82, v86, s0
	v_perm_b32 v82, v82, v86, s1
	v_pk_fma_f16 v86, v87, s36, v103 op_sel_hi:[1,0,1]
	v_pk_fma_f16 v87, v104, s36, v102 op_sel_hi:[1,0,1]
	v_lshrrev_b32_e32 v102, 4, v83
	v_pk_fma_f16 v82, v82, s36, v100 op_sel_hi:[1,0,1]
	v_and_b32_e32 v100, 0x7070707, v83
	v_and_b32_e32 v102, 0x7070707, v102
	v_perm_b32 v100, s2, v205, v100
	v_perm_b32 v102, s2, v205, v102
	v_lshlrev_b32_e32 v103, 4, v83
	v_and_or_b32 v100, v103, s4, v100
	v_and_or_b32 v83, v83, s4, v102
	v_perm_b32 v102, v83, v100, s5
	v_perm_b32 v103, v83, v100, s33
	v_perm_b32 v104, v83, v100, s0
	v_perm_b32 v83, v83, v100, s1
	v_readlane_b32 s59, v120, 4
	v_lshrrev_b32_e32 v100, 4, v80
	v_pk_fma_f16 v101, v105, s36, v101 op_sel_hi:[1,0,1]
	v_pk_fma_f16 v99, v102, s36, v99 op_sel_hi:[1,0,1]
	v_pk_fma_f16 v98, v103, s36, v98 op_sel_hi:[1,0,1]
	v_pk_fma_f16 v97, v104, s36, v97 op_sel_hi:[1,0,1]
	v_pk_fma_f16 v83, v83, s36, v96 op_sel_hi:[1,0,1]
	v_and_b32_e32 v96, 0x7070707, v80
	v_and_b32_e32 v100, 0x7070707, v100
	v_perm_b32 v96, s2, v205, v96
	v_perm_b32 v100, s2, v205, v100
	v_lshlrev_b32_e32 v102, 4, v80
	v_and_or_b32 v96, v102, s4, v96
	v_and_or_b32 v80, v80, s4, v100
	v_perm_b32 v100, v80, v96, s5
	v_perm_b32 v102, v80, v96, s33
	v_perm_b32 v103, v80, v96, s0
	v_perm_b32 v80, v80, v96, s1
	v_pk_fma_f16 v86, v100, s59, v86 op_sel_hi:[1,0,1]
	v_lshrrev_b32_e32 v100, 4, v81
	v_pk_fma_f16 v80, v80, s59, v82 op_sel_hi:[1,0,1]
	v_and_b32_e32 v82, 0x7070707, v81
	v_and_b32_e32 v100, 0x7070707, v100
	v_pk_fma_f16 v96, v103, s59, v101 op_sel_hi:[1,0,1]
	v_perm_b32 v82, s2, v205, v82
	v_perm_b32 v100, s2, v205, v100
	v_lshlrev_b32_e32 v101, 4, v81
	v_and_or_b32 v82, v101, s4, v82
	v_and_or_b32 v81, v81, s4, v100
	v_perm_b32 v100, v81, v82, s5
	v_pk_fma_f16 v87, v102, s59, v87 op_sel_hi:[1,0,1]
	v_perm_b32 v101, v81, v82, s33
	v_perm_b32 v102, v81, v82, s0
	v_perm_b32 v81, v81, v82, s1
	v_pk_fma_f16 v82, v100, s59, v99 op_sel_hi:[1,0,1]
	v_readlane_b32 s60, v120, 8
	v_lshrrev_b32_e32 v99, 4, v78
	v_pk_fma_f16 v98, v101, s59, v98 op_sel_hi:[1,0,1]
	v_pk_fma_f16 v97, v102, s59, v97 op_sel_hi:[1,0,1]
	v_pk_fma_f16 v81, v81, s59, v83 op_sel_hi:[1,0,1]
	v_and_b32_e32 v85, 0x7070707, v78
	v_and_b32_e32 v99, 0x7070707, v99
	v_perm_b32 v85, s2, v205, v85
	v_perm_b32 v99, s2, v205, v99
	v_lshlrev_b32_e32 v100, 4, v78
	v_and_or_b32 v85, v100, s4, v85
	v_and_or_b32 v78, v78, s4, v99
	v_perm_b32 v99, v78, v85, s5
	v_perm_b32 v100, v78, v85, s33
	v_perm_b32 v101, v78, v85, s0
	v_perm_b32 v78, v78, v85, s1
	v_pk_fma_f16 v85, v99, s60, v86 op_sel_hi:[1,0,1]
	v_pk_fma_f16 v86, v100, s60, v87 op_sel_hi:[1,0,1]
	v_pk_fma_f16 v87, v101, s60, v96 op_sel_hi:[1,0,1]
	v_lshrrev_b32_e32 v96, 4, v79
	v_pk_fma_f16 v78, v78, s60, v80 op_sel_hi:[1,0,1]
	v_and_b32_e32 v80, 0x7070707, v79
	v_and_b32_e32 v96, 0x7070707, v96
	v_perm_b32 v80, s2, v205, v80
	v_perm_b32 v96, s2, v205, v96
	v_lshlrev_b32_e32 v99, 4, v79
	v_and_or_b32 v80, v99, s4, v80
	v_and_or_b32 v79, v79, s4, v96
	v_perm_b32 v96, v79, v80, s5
	v_perm_b32 v100, v79, v80, s0
	v_perm_b32 v99, v79, v80, s33
	v_perm_b32 v79, v79, v80, s1
	v_pk_fma_f16 v80, v96, s60, v82 op_sel_hi:[1,0,1]
	v_pk_fma_f16 v96, v100, s60, v97 op_sel_hi:[1,0,1]
	v_readlane_b32 s36, v120, 12
	v_lshrrev_b32_e32 v97, 4, v76
	v_pk_fma_f16 v82, v99, s60, v98 op_sel_hi:[1,0,1]
	v_pk_fma_f16 v79, v79, s60, v81 op_sel_hi:[1,0,1]
	v_and_b32_e32 v83, 0x7070707, v76
	v_and_b32_e32 v97, 0x7070707, v97
	v_perm_b32 v83, s2, v205, v83
	v_perm_b32 v97, s2, v205, v97
	v_lshlrev_b32_e32 v98, 4, v76
	v_and_or_b32 v83, v98, s4, v83
	v_and_or_b32 v76, v76, s4, v97
	v_perm_b32 v97, v76, v83, s5
	v_perm_b32 v98, v76, v83, s33
	v_perm_b32 v99, v76, v83, s0
	v_perm_b32 v76, v76, v83, s1
	v_pk_fma_f16 v83, v97, s36, v85 op_sel_hi:[1,0,1]
	v_pk_fma_f16 v85, v98, s36, v86 op_sel_hi:[1,0,1]
	v_pk_fma_f16 v86, v99, s36, v87 op_sel_hi:[1,0,1]
	v_lshrrev_b32_e32 v87, 4, v77
	v_pk_fma_f16 v76, v76, s36, v78 op_sel_hi:[1,0,1]
	v_and_b32_e32 v78, 0x7070707, v77
	v_and_b32_e32 v87, 0x7070707, v87
	v_perm_b32 v78, s2, v205, v78
	v_perm_b32 v87, s2, v205, v87
	v_lshlrev_b32_e32 v97, 4, v77
	v_and_or_b32 v78, v97, s4, v78
	v_and_or_b32 v77, v77, s4, v87
	v_perm_b32 v87, v77, v78, s5
	v_perm_b32 v97, v77, v78, s33
	v_perm_b32 v98, v77, v78, s0
	v_perm_b32 v77, v77, v78, s1
	v_pk_fma_f16 v78, v87, s36, v80 op_sel_hi:[1,0,1]
	v_readlane_b32 s59, v120, 16
	v_lshrrev_b32_e32 v87, 4, v74
	v_pk_fma_f16 v80, v97, s36, v82 op_sel_hi:[1,0,1]
	v_pk_fma_f16 v82, v98, s36, v96 op_sel_hi:[1,0,1]
	v_pk_fma_f16 v77, v77, s36, v79 op_sel_hi:[1,0,1]
	v_and_b32_e32 v81, 0x7070707, v74
	v_and_b32_e32 v87, 0x7070707, v87
	v_perm_b32 v81, s2, v205, v81
	v_perm_b32 v87, s2, v205, v87
	v_lshlrev_b32_e32 v96, 4, v74
	v_and_or_b32 v81, v96, s4, v81
	v_and_or_b32 v74, v74, s4, v87
	v_perm_b32 v87, v74, v81, s5
	v_perm_b32 v96, v74, v81, s33
	v_perm_b32 v97, v74, v81, s0
	v_perm_b32 v74, v74, v81, s1
	v_pk_fma_f16 v81, v87, s59, v83 op_sel_hi:[1,0,1]
	v_pk_fma_f16 v83, v96, s59, v85 op_sel_hi:[1,0,1]
	v_pk_fma_f16 v85, v97, s59, v86 op_sel_hi:[1,0,1]
	v_lshrrev_b32_e32 v86, 4, v75
	v_pk_fma_f16 v74, v74, s59, v76 op_sel_hi:[1,0,1]
	v_and_b32_e32 v76, 0x7070707, v75
	v_and_b32_e32 v86, 0x7070707, v86
	v_perm_b32 v76, s2, v205, v76
	v_perm_b32 v86, s2, v205, v86
	v_lshlrev_b32_e32 v87, 4, v75
	v_and_or_b32 v76, v87, s4, v76
	v_and_or_b32 v75, v75, s4, v86
	v_perm_b32 v86, v75, v76, s5
	v_perm_b32 v87, v75, v76, s33
	v_perm_b32 v96, v75, v76, s0
	v_perm_b32 v75, v75, v76, s1
	v_pk_fma_f16 v76, v86, s59, v78 op_sel_hi:[1,0,1]
	v_pk_fma_f16 v78, v87, s59, v80 op_sel_hi:[1,0,1]
	v_pk_fma_f16 v80, v96, s59, v82 op_sel_hi:[1,0,1]
	v_readlane_b32 s60, v120, 20
	v_lshrrev_b32_e32 v82, 4, v70
	v_pk_fma_f16 v75, v75, s59, v77 op_sel_hi:[1,0,1]
	v_and_b32_e32 v79, 0x7070707, v70
	v_and_b32_e32 v82, 0x7070707, v82
	v_perm_b32 v79, s2, v205, v79
	v_perm_b32 v82, s2, v205, v82
	v_lshlrev_b32_e32 v86, 4, v70
	v_and_or_b32 v79, v86, s4, v79
	v_and_or_b32 v70, v70, s4, v82
	v_perm_b32 v82, v70, v79, s5
	v_perm_b32 v86, v70, v79, s33
	v_perm_b32 v87, v70, v79, s0
	v_perm_b32 v70, v70, v79, s1
	v_pk_fma_f16 v79, v82, s60, v81 op_sel_hi:[1,0,1]
	v_pk_fma_f16 v81, v86, s60, v83 op_sel_hi:[1,0,1]
	v_lshrrev_b32_e32 v83, 4, v71
	v_pk_fma_f16 v70, v70, s60, v74 op_sel_hi:[1,0,1]
	v_and_b32_e32 v74, 0x7070707, v71
	v_and_b32_e32 v83, 0x7070707, v83
	v_pk_fma_f16 v82, v87, s60, v85 op_sel_hi:[1,0,1]
	v_perm_b32 v74, s2, v205, v74
	v_perm_b32 v83, s2, v205, v83
	v_lshlrev_b32_e32 v85, 4, v71
	v_and_or_b32 v74, v85, s4, v74
	v_and_or_b32 v71, v71, s4, v83
	v_perm_b32 v83, v71, v74, s5
	v_perm_b32 v85, v71, v74, s33
	v_perm_b32 v86, v71, v74, s0
	v_perm_b32 v71, v71, v74, s1
	v_pk_fma_f16 v74, v83, s60, v76 op_sel_hi:[1,0,1]
	v_pk_fma_f16 v76, v85, s60, v78 op_sel_hi:[1,0,1]
	v_pk_fma_f16 v78, v86, s60, v80 op_sel_hi:[1,0,1]
	v_readlane_b32 s36, v120, 24
	v_lshrrev_b32_e32 v80, 4, v68
	v_pk_fma_f16 v71, v71, s60, v75 op_sel_hi:[1,0,1]
	v_and_b32_e32 v77, 0x7070707, v68
	v_and_b32_e32 v80, 0x7070707, v80
	v_perm_b32 v77, s2, v205, v77
	v_perm_b32 v80, s2, v205, v80
	v_lshlrev_b32_e32 v83, 4, v68
	v_and_or_b32 v77, v83, s4, v77
	v_and_or_b32 v68, v68, s4, v80
	v_perm_b32 v80, v68, v77, s5
	v_perm_b32 v83, v68, v77, s33
	v_perm_b32 v85, v68, v77, s0
	v_perm_b32 v68, v68, v77, s1
	v_pk_fma_f16 v77, v80, s36, v79 op_sel_hi:[1,0,1]
	v_pk_fma_f16 v79, v83, s36, v81 op_sel_hi:[1,0,1]
	v_lshrrev_b32_e32 v81, 4, v69
	v_pk_fma_f16 v68, v68, s36, v70 op_sel_hi:[1,0,1]
	v_and_b32_e32 v70, 0x7070707, v69
	v_and_b32_e32 v81, 0x7070707, v81
	v_pk_fma_f16 v80, v85, s36, v82 op_sel_hi:[1,0,1]
	v_perm_b32 v70, s2, v205, v70
	v_perm_b32 v81, s2, v205, v81
	v_lshlrev_b32_e32 v82, 4, v69
	v_and_or_b32 v70, v82, s4, v70
	v_and_or_b32 v69, v69, s4, v81
	v_perm_b32 v81, v69, v70, s5
	v_perm_b32 v82, v69, v70, s33
	v_perm_b32 v83, v69, v70, s0
	v_perm_b32 v69, v69, v70, s1
	v_pk_fma_f16 v70, v81, s36, v74 op_sel_hi:[1,0,1]
	v_pk_fma_f16 v74, v82, s36, v76 op_sel_hi:[1,0,1]
	v_pk_fma_f16 v76, v83, s36, v78 op_sel_hi:[1,0,1]
	v_readlane_b32 s59, v120, 28
	v_lshrrev_b32_e32 v78, 4, v64
	v_pk_fma_f16 v69, v69, s36, v71 op_sel_hi:[1,0,1]
	v_and_b32_e32 v75, 0x7070707, v64
	v_and_b32_e32 v78, 0x7070707, v78
	v_perm_b32 v75, s2, v205, v75
	v_perm_b32 v78, s2, v205, v78
	v_lshlrev_b32_e32 v81, 4, v64
	v_and_or_b32 v75, v81, s4, v75
	v_and_or_b32 v64, v64, s4, v78
	v_perm_b32 v78, v64, v75, s5
	v_perm_b32 v81, v64, v75, s33
	v_perm_b32 v82, v64, v75, s0
	v_perm_b32 v64, v64, v75, s1
	v_pk_fma_f16 v75, v78, s59, v77 op_sel_hi:[1,0,1]
	v_pk_fma_f16 v77, v81, s59, v79 op_sel_hi:[1,0,1]
	v_lshrrev_b32_e32 v79, 4, v65
	v_pk_fma_f16 v64, v64, s59, v68 op_sel_hi:[1,0,1]
	v_and_b32_e32 v68, 0x7070707, v65
	v_and_b32_e32 v79, 0x7070707, v79
	v_pk_fma_f16 v78, v82, s59, v80 op_sel_hi:[1,0,1]
	v_perm_b32 v68, s2, v205, v68
	v_perm_b32 v79, s2, v205, v79
	v_lshlrev_b32_e32 v80, 4, v65
	v_and_or_b32 v68, v80, s4, v68
	v_and_or_b32 v65, v65, s4, v79
	v_perm_b32 v79, v65, v68, s5
	v_perm_b32 v80, v65, v68, s33
	v_perm_b32 v81, v65, v68, s0
	v_perm_b32 v65, v65, v68, s1
	v_pk_fma_f16 v68, v79, s59, v70 op_sel_hi:[1,0,1]
	v_pk_fma_f16 v70, v80, s59, v74 op_sel_hi:[1,0,1]
	v_pk_fma_f16 v74, v81, s59, v76 op_sel_hi:[1,0,1]
	v_readlane_b32 s60, v120, 32
	v_lshrrev_b32_e32 v76, 4, v62
	v_pk_fma_f16 v65, v65, s59, v69 op_sel_hi:[1,0,1]
	v_and_b32_e32 v71, 0x7070707, v62
	v_and_b32_e32 v76, 0x7070707, v76
	v_perm_b32 v71, s2, v205, v71
	v_perm_b32 v76, s2, v205, v76
	v_lshlrev_b32_e32 v79, 4, v62
	v_and_or_b32 v71, v79, s4, v71
	v_and_or_b32 v62, v62, s4, v76
	v_perm_b32 v76, v62, v71, s5
	v_perm_b32 v79, v62, v71, s33
	v_perm_b32 v80, v62, v71, s0
	v_perm_b32 v62, v62, v71, s1
	v_pk_fma_f16 v71, v76, s60, v75 op_sel_hi:[1,0,1]
	v_pk_fma_f16 v75, v79, s60, v77 op_sel_hi:[1,0,1]
	v_lshrrev_b32_e32 v77, 4, v63
	v_pk_fma_f16 v62, v62, s60, v64 op_sel_hi:[1,0,1]
	v_and_b32_e32 v64, 0x7070707, v63
	v_and_b32_e32 v77, 0x7070707, v77
	v_pk_fma_f16 v76, v80, s60, v78 op_sel_hi:[1,0,1]
	v_perm_b32 v64, s2, v205, v64
	v_perm_b32 v77, s2, v205, v77
	v_lshlrev_b32_e32 v78, 4, v63
	v_and_or_b32 v64, v78, s4, v64
	v_and_or_b32 v63, v63, s4, v77
	v_perm_b32 v77, v63, v64, s5
	v_perm_b32 v78, v63, v64, s33
	v_perm_b32 v79, v63, v64, s0
	v_perm_b32 v63, v63, v64, s1
	v_pk_fma_f16 v64, v77, s60, v68 op_sel_hi:[1,0,1]
	v_pk_fma_f16 v68, v78, s60, v70 op_sel_hi:[1,0,1]
	v_pk_fma_f16 v70, v79, s60, v74 op_sel_hi:[1,0,1]
	v_readlane_b32 s36, v120, 36
	v_lshrrev_b32_e32 v74, 4, v66
	v_pk_fma_f16 v63, v63, s60, v65 op_sel_hi:[1,0,1]
	v_and_b32_e32 v69, 0x7070707, v66
	v_and_b32_e32 v74, 0x7070707, v74
	v_perm_b32 v69, s2, v205, v69
	v_perm_b32 v74, s2, v205, v74
	v_lshlrev_b32_e32 v77, 4, v66
	v_and_or_b32 v69, v77, s4, v69
	v_and_or_b32 v66, v66, s4, v74
	v_perm_b32 v74, v66, v69, s5
	v_perm_b32 v77, v66, v69, s33
	v_perm_b32 v78, v66, v69, s0
	v_perm_b32 v66, v66, v69, s1
	v_pk_fma_f16 v69, v74, s36, v71 op_sel_hi:[1,0,1]
	v_pk_fma_f16 v71, v77, s36, v75 op_sel_hi:[1,0,1]
	v_lshrrev_b32_e32 v75, 4, v67
	v_pk_fma_f16 v62, v66, s36, v62 op_sel_hi:[1,0,1]
	v_and_b32_e32 v66, 0x7070707, v67
	v_and_b32_e32 v75, 0x7070707, v75
	v_pk_fma_f16 v74, v78, s36, v76 op_sel_hi:[1,0,1]
	v_perm_b32 v66, s2, v205, v66
	v_perm_b32 v75, s2, v205, v75
	v_lshlrev_b32_e32 v76, 4, v67
	v_and_or_b32 v66, v76, s4, v66
	v_and_or_b32 v67, v67, s4, v75
	v_perm_b32 v76, v67, v66, s33
	v_perm_b32 v77, v67, v66, s0
	v_perm_b32 v75, v67, v66, s5
	v_perm_b32 v66, v67, v66, s1
	v_pk_fma_f16 v67, v76, s36, v68 op_sel_hi:[1,0,1]
	v_pk_fma_f16 v68, v77, s36, v70 op_sel_hi:[1,0,1]
	v_readlane_b32 s59, v120, 40
	v_lshrrev_b32_e32 v70, 4, v60
	v_pk_fma_f16 v64, v75, s36, v64 op_sel_hi:[1,0,1]
	v_pk_fma_f16 v63, v66, s36, v63 op_sel_hi:[1,0,1]
	v_and_b32_e32 v66, 0x7070707, v60
	v_and_b32_e32 v70, 0x7070707, v70
	v_perm_b32 v66, s2, v205, v66
	v_perm_b32 v70, s2, v205, v70
	v_lshlrev_b32_e32 v75, 4, v60
	v_and_or_b32 v66, v75, s4, v66
	v_and_or_b32 v60, v60, s4, v70
	v_perm_b32 v70, v60, v66, s5
	v_perm_b32 v75, v60, v66, s33
	v_perm_b32 v76, v60, v66, s0
	v_perm_b32 v60, v60, v66, s1
	v_pk_fma_f16 v66, v70, s59, v69 op_sel_hi:[1,0,1]
	v_pk_fma_f16 v69, v75, s59, v71 op_sel_hi:[1,0,1]
	v_lshrrev_b32_e32 v71, 4, v61
	v_pk_fma_f16 v60, v60, s59, v62 op_sel_hi:[1,0,1]
	v_and_b32_e32 v62, 0x7070707, v61
	v_and_b32_e32 v71, 0x7070707, v71
	v_pk_fma_f16 v70, v76, s59, v74 op_sel_hi:[1,0,1]
	v_perm_b32 v62, s2, v205, v62
	v_perm_b32 v71, s2, v205, v71
	v_lshlrev_b32_e32 v74, 4, v61
	v_and_or_b32 v62, v74, s4, v62
	v_and_or_b32 v61, v61, s4, v71
	v_perm_b32 v71, v61, v62, s5
	v_perm_b32 v74, v61, v62, s33
	v_perm_b32 v75, v61, v62, s0
	v_perm_b32 v61, v61, v62, s1
	v_pk_fma_f16 v62, v71, s59, v64 op_sel_hi:[1,0,1]
	v_pk_fma_f16 v64, v74, s59, v67 op_sel_hi:[1,0,1]
	v_pk_fma_f16 v67, v75, s59, v68 op_sel_hi:[1,0,1]
	v_readlane_b32 s60, v120, 44
	v_lshrrev_b32_e32 v68, 4, v58
	v_pk_fma_f16 v61, v61, s59, v63 op_sel_hi:[1,0,1]
	v_and_b32_e32 v65, 0x7070707, v58
	v_and_b32_e32 v68, 0x7070707, v68
	v_perm_b32 v65, s2, v205, v65
	v_perm_b32 v68, s2, v205, v68
	v_lshlrev_b32_e32 v71, 4, v58
	v_and_or_b32 v65, v71, s4, v65
	v_and_or_b32 v58, v58, s4, v68
	v_perm_b32 v68, v58, v65, s5
	v_perm_b32 v71, v58, v65, s33
	v_perm_b32 v74, v58, v65, s0
	v_perm_b32 v58, v58, v65, s1
	v_pk_fma_f16 v65, v68, s60, v66 op_sel_hi:[1,0,1]
	v_pk_fma_f16 v66, v71, s60, v69 op_sel_hi:[1,0,1]
	v_lshrrev_b32_e32 v69, 4, v59
	v_pk_fma_f16 v58, v58, s60, v60 op_sel_hi:[1,0,1]
	v_and_b32_e32 v60, 0x7070707, v59
	v_and_b32_e32 v69, 0x7070707, v69
	v_pk_fma_f16 v68, v74, s60, v70 op_sel_hi:[1,0,1]
	v_perm_b32 v60, s2, v205, v60
	v_perm_b32 v69, s2, v205, v69
	v_lshlrev_b32_e32 v70, 4, v59
	v_and_or_b32 v60, v70, s4, v60
	v_and_or_b32 v59, v59, s4, v69
	v_perm_b32 v69, v59, v60, s5
	v_perm_b32 v70, v59, v60, s33
	v_perm_b32 v71, v59, v60, s0
	v_perm_b32 v59, v59, v60, s1
	v_pk_fma_f16 v60, v69, s60, v62 op_sel_hi:[1,0,1]
	v_pk_fma_f16 v62, v70, s60, v64 op_sel_hi:[1,0,1]
	v_pk_fma_f16 v64, v71, s60, v67 op_sel_hi:[1,0,1]
	v_readlane_b32 s36, v120, 48
	v_lshrrev_b32_e32 v67, 4, v56
	v_pk_fma_f16 v59, v59, s60, v61 op_sel_hi:[1,0,1]
	v_and_b32_e32 v63, 0x7070707, v56
	v_and_b32_e32 v67, 0x7070707, v67
	v_perm_b32 v63, s2, v205, v63
	v_perm_b32 v67, s2, v205, v67
	v_lshlrev_b32_e32 v69, 4, v56
	v_and_or_b32 v63, v69, s4, v63
	v_and_or_b32 v56, v56, s4, v67
	v_perm_b32 v67, v56, v63, s5
	v_perm_b32 v69, v56, v63, s33
	v_perm_b32 v70, v56, v63, s0
	v_perm_b32 v56, v56, v63, s1
	v_pk_fma_f16 v63, v67, s36, v65 op_sel_hi:[1,0,1]
	v_lshrrev_b32_e32 v67, 4, v57
	v_pk_fma_f16 v56, v56, s36, v58 op_sel_hi:[1,0,1]
	v_and_b32_e32 v58, 0x7070707, v57
	v_and_b32_e32 v67, 0x7070707, v67
	v_pk_fma_f16 v65, v69, s36, v66 op_sel_hi:[1,0,1]
	v_pk_fma_f16 v66, v70, s36, v68 op_sel_hi:[1,0,1]
	v_perm_b32 v58, s2, v205, v58
	v_perm_b32 v67, s2, v205, v67
	v_lshlrev_b32_e32 v68, 4, v57
	v_and_or_b32 v58, v68, s4, v58
	v_and_or_b32 v57, v57, s4, v67
	v_perm_b32 v67, v57, v58, s5
	v_perm_b32 v68, v57, v58, s33
	v_perm_b32 v69, v57, v58, s0
	v_perm_b32 v57, v57, v58, s1
	v_pk_fma_f16 v58, v67, s36, v60 op_sel_hi:[1,0,1]
	v_pk_fma_f16 v60, v68, s36, v62 op_sel_hi:[1,0,1]
	v_pk_fma_f16 v62, v69, s36, v64 op_sel_hi:[1,0,1]
	v_readlane_b32 s59, v120, 52
	v_lshrrev_b32_e32 v64, 4, v54
	v_pk_fma_f16 v57, v57, s36, v59 op_sel_hi:[1,0,1]
	v_and_b32_e32 v61, 0x7070707, v54
	v_and_b32_e32 v64, 0x7070707, v64
	v_perm_b32 v61, s2, v205, v61
	v_perm_b32 v64, s2, v205, v64
	v_lshlrev_b32_e32 v67, 4, v54
	v_and_or_b32 v61, v67, s4, v61
	v_and_or_b32 v54, v54, s4, v64
	v_perm_b32 v64, v54, v61, s5
	v_perm_b32 v67, v54, v61, s33
	v_perm_b32 v68, v54, v61, s0
	v_perm_b32 v54, v54, v61, s1
	v_pk_fma_f16 v61, v64, s59, v63 op_sel_hi:[1,0,1]
	v_pk_fma_f16 v63, v67, s59, v65 op_sel_hi:[1,0,1]
	v_lshrrev_b32_e32 v65, 4, v55
	v_pk_fma_f16 v54, v54, s59, v56 op_sel_hi:[1,0,1]
	v_and_b32_e32 v56, 0x7070707, v55
	v_and_b32_e32 v65, 0x7070707, v65
	v_pk_fma_f16 v64, v68, s59, v66 op_sel_hi:[1,0,1]
	v_perm_b32 v56, s2, v205, v56
	v_perm_b32 v65, s2, v205, v65
	v_lshlrev_b32_e32 v66, 4, v55
	v_and_or_b32 v56, v66, s4, v56
	v_and_or_b32 v55, v55, s4, v65
	v_perm_b32 v65, v55, v56, s5
	v_perm_b32 v66, v55, v56, s33
	v_perm_b32 v67, v55, v56, s0
	v_perm_b32 v55, v55, v56, s1
	v_pk_fma_f16 v56, v65, s59, v58 op_sel_hi:[1,0,1]
	v_pk_fma_f16 v58, v66, s59, v60 op_sel_hi:[1,0,1]
	v_pk_fma_f16 v60, v67, s59, v62 op_sel_hi:[1,0,1]
	v_readlane_b32 s60, v120, 56
	v_lshrrev_b32_e32 v62, 4, v52
	v_pk_fma_f16 v55, v55, s59, v57 op_sel_hi:[1,0,1]
	v_and_b32_e32 v59, 0x7070707, v52
	v_and_b32_e32 v62, 0x7070707, v62
	v_perm_b32 v59, s2, v205, v59
	v_perm_b32 v62, s2, v205, v62
	v_lshlrev_b32_e32 v65, 4, v52
	v_and_or_b32 v59, v65, s4, v59
	v_and_or_b32 v52, v52, s4, v62
	v_perm_b32 v62, v52, v59, s5
	v_perm_b32 v65, v52, v59, s33
	v_perm_b32 v66, v52, v59, s0
	v_perm_b32 v52, v52, v59, s1
	v_pk_fma_f16 v59, v62, s60, v61 op_sel_hi:[1,0,1]
	v_pk_fma_f16 v61, v65, s60, v63 op_sel_hi:[1,0,1]
	v_lshrrev_b32_e32 v63, 4, v53
	v_pk_fma_f16 v52, v52, s60, v54 op_sel_hi:[1,0,1]
	v_and_b32_e32 v54, 0x7070707, v53
	v_and_b32_e32 v63, 0x7070707, v63
	v_pk_fma_f16 v62, v66, s60, v64 op_sel_hi:[1,0,1]
	v_perm_b32 v54, s2, v205, v54
	v_perm_b32 v63, s2, v205, v63
	v_lshlrev_b32_e32 v64, 4, v53
	v_and_or_b32 v54, v64, s4, v54
	v_and_or_b32 v53, v53, s4, v63
	v_perm_b32 v63, v53, v54, s5
	v_perm_b32 v64, v53, v54, s33
	v_perm_b32 v65, v53, v54, s0
	v_perm_b32 v53, v53, v54, s1
	v_pk_fma_f16 v54, v63, s60, v56 op_sel_hi:[1,0,1]
	v_pk_fma_f16 v56, v64, s60, v58 op_sel_hi:[1,0,1]
	v_pk_fma_f16 v58, v65, s60, v60 op_sel_hi:[1,0,1]
	v_readlane_b32 s36, v120, 60
	v_lshrrev_b32_e32 v60, 4, v36
	v_pk_fma_f16 v53, v53, s60, v55 op_sel_hi:[1,0,1]
	v_and_b32_e32 v57, 0x7070707, v36
	v_and_b32_e32 v60, 0x7070707, v60
	v_perm_b32 v57, s2, v205, v57
	v_perm_b32 v60, s2, v205, v60
	v_lshlrev_b32_e32 v63, 4, v36
	v_and_or_b32 v57, v63, s4, v57
	v_and_or_b32 v36, v36, s4, v60
	v_perm_b32 v60, v36, v57, s5
	v_perm_b32 v63, v36, v57, s33
	v_perm_b32 v64, v36, v57, s0
	v_perm_b32 v36, v36, v57, s1
	v_pk_fma_f16 v100, v36, s36, v52 op_sel_hi:[1,0,1]
	v_lshrrev_b32_e32 v52, 4, v37
	v_and_b32_e32 v36, 0x7070707, v37
	v_and_b32_e32 v52, 0x7070707, v52
	v_perm_b32 v36, s2, v205, v36
	v_perm_b32 v52, s2, v205, v52
	v_lshlrev_b32_e32 v57, 4, v37
	v_and_or_b32 v36, v57, s4, v36
	v_and_or_b32 v37, v37, s4, v52
	v_pk_fma_f16 v103, v60, s36, v59 op_sel_hi:[1,0,1]
	v_perm_b32 v52, v37, v36, s5
	v_perm_b32 v57, v37, v36, s33
	v_perm_b32 v59, v37, v36, s0
	v_perm_b32 v36, v37, v36, s1
	v_pk_fma_f16 v96, v36, s36, v53 op_sel_hi:[1,0,1]
	v_lshl_add_u64 v[36:37], v[6:7], 0, s[12:13]
	global_load_dwordx2 v[82:83], v[36:37], off
	v_lshl_add_u64 v[36:37], v[6:7], 0, s[14:15]
	global_load_dwordx2 v[80:81], v[36:37], off
	v_lshl_add_u64 v[40:41], v[4:5], 0, s[38:39]
	v_lshl_add_u64 v[36:37], v[6:7], 0, s[16:17]
	global_load_dwordx2 v[48:49], v[40:41], off
	global_load_dwordx2 v[78:79], v[36:37], off
	v_lshl_add_u64 v[40:41], v[4:5], 0, s[50:51]
	v_lshl_add_u64 v[36:37], v[6:7], 0, s[18:19]
	global_load_dwordx2 v[46:47], v[40:41], off
	global_load_dwordx2 v[76:77], v[36:37], off
	v_lshl_add_u64 v[40:41], v[4:5], 0, s[52:53]
	v_lshl_add_u64 v[36:37], v[6:7], 0, s[20:21]
	global_load_dwordx2 v[44:45], v[40:41], off
	global_load_dwordx2 v[74:75], v[36:37], off
	v_lshl_add_u64 v[40:41], v[4:5], 0, s[54:55]
	v_lshl_add_u64 v[36:37], v[6:7], 0, s[22:23]
	global_load_dwordx2 v[42:43], v[40:41], off
	global_load_dwordx2 v[70:71], v[36:37], off
	v_lshl_add_u64 v[40:41], v[4:5], 0, s[56:57]
	v_lshl_add_u64 v[36:37], v[6:7], 0, s[24:25]
	global_load_dwordx2 v[40:41], v[40:41], off
	v_pk_fma_f16 v101, v64, s36, v62 op_sel_hi:[1,0,1]
	global_load_dwordx2 v[68:69], v[36:37], off
	v_lshl_add_u64 v[36:37], v[6:7], 0, s[26:27]
	global_load_dwordx2 v[64:65], v[36:37], off
	v_lshl_add_u64 v[36:37], v[6:7], 0, s[28:29]
	v_pk_fma_f16 v102, v63, s36, v61 op_sel_hi:[1,0,1]
	global_load_dwordx2 v[62:63], v[36:37], off
	v_lshl_add_u64 v[36:37], v[6:7], 0, s[30:31]
	global_load_dwordx2 v[66:67], v[36:37], off
	v_lshl_add_u64 v[36:37], v[6:7], 0, s[34:35]
	global_load_dwordx2 v[60:61], v[36:37], off
	v_lshl_add_u64 v[36:37], v[6:7], 0, s[38:39]
	v_pk_fma_f16 v97, v59, s36, v58 op_sel_hi:[1,0,1]
	global_load_dwordx2 v[58:59], v[36:37], off
	v_lshl_add_u64 v[36:37], v[6:7], 0, s[50:51]
	v_pk_fma_f16 v98, v57, s36, v56 op_sel_hi:[1,0,1]
	global_load_dwordx2 v[56:57], v[36:37], off
	v_lshl_add_u64 v[36:37], v[6:7], 0, s[52:53]
	v_pk_fma_f16 v99, v52, s36, v54 op_sel_hi:[1,0,1]
	global_load_dwordx2 v[54:55], v[36:37], off
	v_lshl_add_u64 v[36:37], v[6:7], 0, s[54:55]
	global_load_dwordx2 v[52:53], v[36:37], off
	v_lshl_add_u64 v[36:37], v[6:7], 0, s[56:57]
	global_load_dwordx2 v[8:9], v[8:9], off
	s_cmpk_eq_i32 s58, 0x90
	global_load_dwordx2 v[10:11], v[10:11], off
	s_nop 0
	global_load_dwordx2 v[12:13], v[12:13], off
	s_nop 0
	global_load_dwordx2 v[14:15], v[14:15], off
	s_nop 0
	global_load_dwordx2 v[16:17], v[16:17], off
	s_nop 0
	global_load_dwordx2 v[18:19], v[18:19], off
	s_nop 0
	global_load_dwordx2 v[20:21], v[20:21], off
	s_nop 0
	global_load_dwordx2 v[22:23], v[22:23], off
	s_nop 0
	global_load_dwordx2 v[36:37], v[36:37], off
	s_cbranch_scc0 .LBB0_763
	v_lshlrev_b64 v[0:1], 2, v[2:3]
	v_lshl_add_u64 v[2:3], v[28:29], 0, v[0:1]
	global_load_dwordx4 v[104:107], v[2:3], off offset:48
	global_load_dwordx4 v[108:111], v[2:3], off offset:32
	global_load_dwordx4 v[86:89], v[2:3], off offset:16
	global_load_dwordx4 v[112:115], v[2:3], off
	v_lshl_add_u64 v[72:73], v[32:33], 0, v[0:1]
	v_cvt_f32_f16_sdwa v1, v103 dst_sel:DWORD dst_unused:UNUSED_PAD src0_sel:WORD_1
	v_cvt_f32_f16_e32 v0, v103
	v_cvt_f32_f16_sdwa v91, v102 dst_sel:DWORD dst_unused:UNUSED_PAD src0_sel:WORD_1
	v_cvt_f32_f16_e32 v90, v102
	v_cvt_f32_f16_sdwa v103, v101 dst_sel:DWORD dst_unused:UNUSED_PAD src0_sel:WORD_1
	v_cvt_f32_f16_e32 v102, v101
	v_cvt_f32_f16_sdwa v101, v100 dst_sel:DWORD dst_unused:UNUSED_PAD src0_sel:WORD_1
	v_cvt_f32_f16_e32 v100, v100
	s_mov_b32 s18, 0x800000
	v_readlane_b32 s12, v255, 5
	v_readlane_b32 s13, v255, 6
	s_waitcnt vmcnt(1)
	v_pk_add_f32 v[86:87], v[86:87], v[102:103]
	s_waitcnt vmcnt(0)
	v_pk_add_f32 v[84:85], v[112:113], v[0:1]
	global_load_dwordx4 v[0:3], v[30:31], off
	v_mov_b32_e32 v102, v85
	v_mov_b32_e32 v103, v87
	v_pk_add_f32 v[90:91], v[114:115], v[90:91]
	v_pk_add_f32 v[88:89], v[88:89], v[100:101]
	v_mov_b32_e32 v100, v84
	v_mov_b32_e32 v101, v86
	v_pk_mul_f32 v[102:103], v[102:103], v[102:103]
	v_mov_b32_e32 v112, v91
	v_pk_fma_f32 v[100:101], v[100:101], v[100:101], v[102:103]
	v_mov_b32_e32 v102, v90
	v_mov_b32_e32 v103, v88
	v_pk_fma_f32 v[100:101], v[102:103], v[102:103], v[100:101]
	v_cvt_f32_f16_sdwa v103, v99 dst_sel:DWORD dst_unused:UNUSED_PAD src0_sel:WORD_1
	v_cvt_f32_f16_e32 v102, v99
	v_cvt_f32_f16_sdwa v99, v98 dst_sel:DWORD dst_unused:UNUSED_PAD src0_sel:WORD_1
	v_cvt_f32_f16_e32 v98, v98
	v_mov_b32_e32 v113, v89
	v_pk_add_f32 v[102:103], v[108:109], v[102:103]
	v_cvt_f32_f16_sdwa v109, v97 dst_sel:DWORD dst_unused:UNUSED_PAD src0_sel:WORD_1
	v_cvt_f32_f16_e32 v108, v97
	v_cvt_f32_f16_sdwa v97, v96 dst_sel:DWORD dst_unused:UNUSED_PAD src0_sel:WORD_1
	v_cvt_f32_f16_e32 v96, v96
	v_pk_add_f32 v[98:99], v[110:111], v[98:99]
	v_pk_add_f32 v[104:105], v[104:105], v[108:109]
	v_mov_b32_e32 v108, v103
	v_mov_b32_e32 v109, v105
	v_pk_add_f32 v[96:97], v[106:107], v[96:97]
	v_mov_b32_e32 v106, v102
	v_mov_b32_e32 v107, v104
	v_pk_mul_f32 v[108:109], v[108:109], v[108:109]
	v_pk_fma_f32 v[100:101], v[112:113], v[112:113], v[100:101]
	v_pk_fma_f32 v[106:107], v[106:107], v[106:107], v[108:109]
	v_mov_b32_e32 v108, v98
	v_mov_b32_e32 v109, v96
	v_mov_b32_e32 v110, v99
	v_mov_b32_e32 v111, v97
	v_pk_fma_f32 v[106:107], v[108:109], v[108:109], v[106:107]
	v_add_f32_e32 v95, v100, v101
	v_pk_fma_f32 v[106:107], v[110:111], v[110:111], v[106:107]
	v_lshl_add_u64 v[34:35], v[34:35], 0, s[12:13]
	v_add_f32_e32 v95, v95, v106
	v_add_f32_e32 v95, v95, v107
	ds_bpermute_b32 v100, v184, v95
	s_waitcnt lgkmcnt(0)
	v_add_f32_e32 v95, v95, v100
	ds_bpermute_b32 v100, v185, v95
	s_waitcnt lgkmcnt(0)
	v_add_f32_e32 v95, v95, v100
	ds_bpermute_b32 v100, v186, v95
	s_waitcnt lgkmcnt(0)
	v_add_f32_e32 v95, v95, v100
	ds_bpermute_b32 v100, v187, v95
	s_waitcnt lgkmcnt(0)
	v_add_f32_e32 v95, v95, v100
	ds_bpermute_b32 v100, v188, v95
	s_waitcnt lgkmcnt(0)
	v_add_f32_e32 v95, v95, v100
	ds_bpermute_b32 v100, v189, v95
	s_waitcnt lgkmcnt(0)
	v_add_f32_e32 v95, v95, v100
	v_fmamk_f32 v95, v95, 0x3a800000, v191
	v_cmp_gt_f32_e32 vcc, s18, v95
	v_mul_f32_e32 v100, 0x4b800000, v95
	s_nop 0
	v_cndmask_b32_e32 v95, v95, v100, vcc
	v_rsq_f32_e32 v95, v95
	s_nop 0
	v_mul_f32_e32 v100, 0x45800000, v95
	v_cndmask_b32_e32 v100, v95, v100, vcc
	v_pk_mul_f32 v[84:85], v[84:85], v[100:101] op_sel_hi:[1,0]
	s_waitcnt vmcnt(0)
	v_pk_mul_f32 v[0:1], v[0:1], v[84:85]
	v_pk_mul_f32 v[84:85], v[90:91], v[100:101] op_sel_hi:[1,0]
	s_nop 0
	v_pk_mul_f32 v[2:3], v[2:3], v[84:85]
	global_store_dwordx4 v[72:73], v[0:3], off
	global_load_dwordx4 v[0:3], v[30:31], off offset:16
	v_pk_mul_f32 v[84:85], v[86:87], v[100:101] op_sel_hi:[1,0]
	s_waitcnt vmcnt(0)
	v_pk_mul_f32 v[0:1], v[0:1], v[84:85]
	v_pk_mul_f32 v[84:85], v[88:89], v[100:101] op_sel_hi:[1,0]
	s_nop 0
	v_pk_mul_f32 v[2:3], v[2:3], v[84:85]
	global_store_dwordx4 v[72:73], v[0:3], off offset:16
	global_load_dwordx4 v[0:3], v[30:31], off offset:32
	v_pk_mul_f32 v[84:85], v[102:103], v[100:101] op_sel_hi:[1,0]
	s_waitcnt vmcnt(0)
	v_pk_mul_f32 v[0:1], v[84:85], v[0:1]
	v_pk_mul_f32 v[84:85], v[98:99], v[100:101] op_sel_hi:[1,0]
	s_nop 0
	v_pk_mul_f32 v[2:3], v[84:85], v[2:3]
	global_store_dwordx4 v[72:73], v[0:3], off offset:32
	global_load_dwordx4 v[0:3], v[30:31], off offset:48
	v_pk_mul_f32 v[84:85], v[104:105], v[100:101] op_sel_hi:[1,0]
	s_waitcnt vmcnt(0)
	v_pk_mul_f32 v[0:1], v[84:85], v[0:1]
	v_pk_mul_f32 v[84:85], v[96:97], v[100:101] op_sel_hi:[1,0]
	s_nop 0
	v_pk_mul_f32 v[2:3], v[84:85], v[2:3]
	global_store_dwordx4 v[72:73], v[0:3], off offset:48
	s_nop 1
	v_mov_b32_e32 v0, v94
	s_andn2_b64 exec, exec, s[10:11]
	s_cbranch_execnz .LBB0_762

.LBB0_770:
	s_cmpk_eq_i32 s56, 0x80
	s_cselect_b64 s[10:11], -1, 0
	ds_bpermute_b32 v6, v97, v96
	s_and_b64 vcc, s[10:11], s[48:49]
	v_cndmask_b32_e32 v94, v0, v98, vcc
	v_ashrrev_i32_e32 v95, 31, v94
	s_and_b32 s10, s56, 0x70
	v_lshlrev_b64 v[94:95], 9, v[94:95]
	v_lshl_add_u64 v[94:95], s[94:95], 0, v[94:95]
	s_lshl_b32 s36, s10, 2
	s_waitcnt lgkmcnt(0)
	v_ashrrev_i32_e32 v7, 31, v6
	v_lshl_add_u64 v[94:95], v[94:95], 0, s[36:37]
	v_lshl_add_u64 v[6:7], v[6:7], 3, s[88:89]
	v_lshl_add_u64 v[94:95], v[94:95], 0, v[144:145]
	global_load_dwordx2 v[6:7], v[6:7], off
	s_nop 0
	global_load_dword v8, v[4:5], off
	global_load_dword v96, v[94:95], off
	s_waitcnt vmcnt(33)
	v_dot8_i32_i4 v9, v20, v1, 0
	v_dot8_i32_i4 v94, v20, v10, 0
	v_dot8_i32_i4 v9, v21, v11, v9
	v_dot8_i32_i4 v94, v21, v12, v94
	v_dot8_i32_i4 v20, v22, v1, 0
	v_dot8_i32_i4 v21, v22, v10, 0
	v_dot8_i32_i4 v20, v23, v11, v20
	v_dot8_i32_i4 v21, v23, v12, v21
	v_lshl_add_u32 v9, v9, 4, v94
	v_cvt_f32_i32_e32 v9, v9
	s_add_i32 s56, s56, 16
	v_lshl_add_u32 v20, v20, 4, v21
	v_cvt_f32_i32_e32 v94, v20
	s_waitcnt vmcnt(32)
	v_dot8_i32_i4 v20, v24, v1, 0
	v_dot8_i32_i4 v21, v24, v10, 0
	v_dot8_i32_i4 v20, v25, v11, v20
	v_dot8_i32_i4 v21, v25, v12, v21
	v_lshl_add_u64 v[4:5], v[4:5], 0, 64
	s_waitcnt vmcnt(2)
	v_mul_f32_e32 v7, v13, v7
	v_lshl_add_u32 v20, v20, 4, v21
	v_cvt_f32_i32_e32 v95, v20
	v_dot8_i32_i4 v20, v26, v1, 0
	v_dot8_i32_i4 v21, v26, v10, 0
	v_dot8_i32_i4 v20, v27, v11, v20
	v_dot8_i32_i4 v21, v27, v12, v21
	s_waitcnt vmcnt(0)
	v_readlane_b32 s10, v96, 0
	s_ashr_i32 s11, s10, 31
	v_readlane_b32 s12, v96, 1
	v_lshl_add_u32 v20, v20, 4, v21
	v_cvt_f32_i32_e32 v106, v20
	v_dot8_i32_i4 v20, v28, v1, 0
	v_dot8_i32_i4 v21, v28, v10, 0
	v_dot8_i32_i4 v20, v29, v11, v20
	v_dot8_i32_i4 v21, v29, v12, v21
	s_lshl_b64 s[10:11], s[10:11], 9
	s_ashr_i32 s13, s12, 31
	v_readlane_b32 s14, v96, 2
	v_lshl_add_u32 v20, v20, 4, v21
	v_cvt_f32_i32_e32 v107, v20
	v_dot8_i32_i4 v20, v30, v1, 0
	v_dot8_i32_i4 v21, v30, v10, 0
	v_dot8_i32_i4 v20, v31, v11, v20
	v_dot8_i32_i4 v21, v31, v12, v21
	s_lshl_b64 s[12:13], s[12:13], 9
	s_ashr_i32 s15, s14, 31
	v_readlane_b32 s16, v96, 3
	v_lshl_add_u32 v20, v20, 4, v21
	v_cvt_f32_i32_e32 v108, v20
	v_dot8_i32_i4 v20, v32, v1, 0
	v_dot8_i32_i4 v21, v32, v10, 0
	v_dot8_i32_i4 v20, v33, v11, v20
	v_dot8_i32_i4 v21, v33, v12, v21
	v_lshl_add_u64 v[22:23], v[16:17], 0, s[12:13]
	s_lshl_b64 s[14:15], s[14:15], 9
	s_ashr_i32 s17, s16, 31
	v_lshl_add_u32 v20, v20, 4, v21
	v_cvt_f32_i32_e32 v109, v20
	v_dot8_i32_i4 v20, v34, v1, 0
	v_dot8_i32_i4 v21, v34, v10, 0
	v_dot8_i32_i4 v20, v35, v11, v20
	v_dot8_i32_i4 v21, v35, v12, v21
	v_readlane_b32 s18, v96, 4
	global_load_dwordx2 v[22:23], v[22:23], off
	v_lshl_add_u64 v[24:25], v[16:17], 0, s[14:15]
	v_lshl_add_u32 v20, v20, 4, v21
	v_cvt_f32_i32_e32 v110, v20
	v_dot8_i32_i4 v20, v36, v1, 0
	v_dot8_i32_i4 v21, v36, v10, 0
	v_dot8_i32_i4 v20, v37, v11, v20
	v_dot8_i32_i4 v21, v37, v12, v21
	s_lshl_b64 s[16:17], s[16:17], 9
	s_ashr_i32 s19, s18, 31
	v_readlane_b32 s20, v96, 5
	v_lshl_add_u32 v20, v20, 4, v21
	v_cvt_f32_i32_e32 v111, v20
	v_dot8_i32_i4 v20, v38, v1, 0
	v_dot8_i32_i4 v21, v38, v10, 0
	v_dot8_i32_i4 v20, v39, v11, v20
	v_dot8_i32_i4 v21, v39, v12, v21
	v_cndmask_b32_e64 v119, v9, v111, s[40:41]
	v_cndmask_b32_e64 v9, v111, v9, s[40:41]
	ds_bpermute_b32 v111, v184, v119
	v_lshl_add_u32 v20, v20, 4, v21
	v_cvt_f32_i32_e32 v112, v20
	v_dot8_i32_i4 v20, v40, v1, 0
	v_dot8_i32_i4 v21, v40, v10, 0
	v_dot8_i32_i4 v20, v41, v11, v20
	v_dot8_i32_i4 v21, v41, v12, v21
	s_waitcnt lgkmcnt(0)
	v_add_f32_e32 v9, v9, v111
	v_cndmask_b32_e64 v111, v94, v112, s[40:41]
	ds_bpermute_b32 v111, v184, v111
	v_lshl_add_u32 v20, v20, 4, v21
	v_cvt_f32_i32_e32 v113, v20
	v_dot8_i32_i4 v20, v60, v1, 0
	v_dot8_i32_i4 v21, v60, v10, 0
	v_cndmask_b32_e64 v94, v112, v94, s[40:41]
	v_dot8_i32_i4 v20, v61, v11, v20
	v_dot8_i32_i4 v21, v61, v12, v21
	s_waitcnt lgkmcnt(0)
	v_add_f32_e32 v94, v94, v111
	v_cndmask_b32_e64 v111, v95, v113, s[40:41]
	ds_bpermute_b32 v111, v184, v111
	v_lshl_add_u32 v20, v20, 4, v21
	v_cvt_f32_i32_e32 v114, v20
	v_dot8_i32_i4 v20, v58, v1, 0
	v_dot8_i32_i4 v21, v58, v10, 0
	v_cndmask_b32_e64 v95, v113, v95, s[40:41]
	v_dot8_i32_i4 v20, v59, v11, v20
	v_dot8_i32_i4 v21, v59, v12, v21
	s_waitcnt lgkmcnt(0)
	v_add_f32_e32 v95, v95, v111
	v_cndmask_b32_e64 v111, v106, v114, s[40:41]
	ds_bpermute_b32 v111, v184, v111
	v_lshl_add_u32 v20, v20, 4, v21
	v_cvt_f32_i32_e32 v115, v20
	v_dot8_i32_i4 v20, v56, v1, 0
	v_dot8_i32_i4 v21, v56, v10, 0
	v_cndmask_b32_e64 v106, v114, v106, s[40:41]
	v_dot8_i32_i4 v20, v57, v11, v20
	v_dot8_i32_i4 v21, v57, v12, v21
	s_waitcnt lgkmcnt(0)
	v_add_f32_e32 v106, v106, v111
	v_cndmask_b32_e64 v111, v107, v115, s[40:41]
	ds_bpermute_b32 v111, v184, v111
	v_lshl_add_u32 v20, v20, 4, v21
	v_cvt_f32_i32_e32 v116, v20
	v_dot8_i32_i4 v20, v54, v1, 0
	v_dot8_i32_i4 v21, v54, v10, 0
	v_cndmask_b32_e64 v107, v115, v107, s[40:41]
	v_dot8_i32_i4 v20, v55, v11, v20
	v_dot8_i32_i4 v21, v55, v12, v21
	s_waitcnt lgkmcnt(0)
	v_add_f32_e32 v107, v107, v111
	v_cndmask_b32_e64 v111, v108, v116, s[40:41]
	ds_bpermute_b32 v111, v184, v111
	v_lshl_add_u32 v20, v20, 4, v21
	v_cvt_f32_i32_e32 v117, v20
	v_dot8_i32_i4 v20, v52, v1, 0
	v_dot8_i32_i4 v21, v52, v10, 0
	v_cndmask_b32_e64 v108, v116, v108, s[40:41]
	v_dot8_i32_i4 v20, v53, v11, v20
	v_dot8_i32_i4 v21, v53, v12, v21
	s_waitcnt lgkmcnt(0)
	v_add_f32_e32 v108, v108, v111
	v_cndmask_b32_e64 v111, v109, v117, s[40:41]
	ds_bpermute_b32 v111, v184, v111
	v_lshl_add_u32 v20, v20, 4, v21
	v_cvt_f32_i32_e32 v118, v20
	v_cndmask_b32_e64 v109, v117, v109, s[40:41]
	v_lshl_add_u64 v[20:21], v[16:17], 0, s[10:11]
	s_waitcnt lgkmcnt(0)
	v_add_f32_e32 v109, v109, v111
	v_cndmask_b32_e64 v111, v110, v118, s[40:41]
	ds_bpermute_b32 v111, v184, v111
	v_cndmask_b32_e64 v110, v118, v110, s[40:41]
	global_load_dwordx2 v[20:21], v[20:21], off
	v_lshl_add_u64 v[26:27], v[16:17], 0, s[16:17]
	global_load_dwordx2 v[24:25], v[24:25], off
	s_waitcnt lgkmcnt(0)
	v_add_f32_e32 v110, v110, v111
	v_cndmask_b32_e64 v111, v9, v107, s[42:43]
	v_cndmask_b32_e64 v9, v107, v9, s[42:43]
	ds_bpermute_b32 v107, v185, v111
	s_lshl_b64 s[18:19], s[18:19], 9
	s_ashr_i32 s21, s20, 31
	v_readlane_b32 s22, v96, 6
	global_load_dwordx2 v[26:27], v[26:27], off
	s_waitcnt lgkmcnt(0)
	v_add_f32_e32 v9, v9, v107
	v_cndmask_b32_e64 v107, v94, v108, s[42:43]
	ds_bpermute_b32 v107, v185, v107
	v_cndmask_b32_e64 v94, v108, v94, s[42:43]
	v_lshl_add_u64 v[28:29], v[16:17], 0, s[18:19]
	s_lshl_b64 s[20:21], s[20:21], 9
	s_ashr_i32 s23, s22, 31
	s_waitcnt lgkmcnt(0)
	v_add_f32_e32 v94, v94, v107
	v_cndmask_b32_e64 v107, v95, v109, s[42:43]
	ds_bpermute_b32 v107, v185, v107
	v_cndmask_b32_e64 v95, v109, v95, s[42:43]
	v_readlane_b32 s24, v96, 7
	global_load_dwordx2 v[28:29], v[28:29], off
	v_lshl_add_u64 v[30:31], v[16:17], 0, s[20:21]
	s_waitcnt lgkmcnt(0)
	v_add_f32_e32 v95, v95, v107
	v_cndmask_b32_e64 v107, v106, v110, s[42:43]
	ds_bpermute_b32 v107, v185, v107
	v_cndmask_b32_e64 v106, v110, v106, s[42:43]
	s_lshl_b64 s[22:23], s[22:23], 9
	s_ashr_i32 s25, s24, 31
	v_readlane_b32 s26, v96, 8
	s_waitcnt lgkmcnt(0)
	v_add_f32_e32 v106, v106, v107
	v_cndmask_b32_e64 v107, v9, v95, s[44:45]
	v_cndmask_b32_e64 v9, v95, v9, s[44:45]
	ds_bpermute_b32 v95, v186, v107
	global_load_dwordx2 v[30:31], v[30:31], off
	v_lshl_add_u64 v[32:33], v[16:17], 0, s[22:23]
	s_lshl_b64 s[24:25], s[24:25], 9
	s_ashr_i32 s27, s26, 31
	s_waitcnt lgkmcnt(0)
	v_add_f32_e32 v9, v9, v95
	v_cndmask_b32_e64 v95, v94, v106, s[44:45]
	ds_bpermute_b32 v95, v186, v95
	v_cndmask_b32_e64 v94, v106, v94, s[44:45]
	v_readlane_b32 s28, v96, 9
	global_load_dwordx2 v[32:33], v[32:33], off
	v_lshl_add_u64 v[34:35], v[16:17], 0, s[24:25]
	s_waitcnt lgkmcnt(0)
	v_add_f32_e32 v94, v94, v95
	v_cndmask_b32_e64 v95, v9, v94, s[46:47]
	v_cndmask_b32_e64 v9, v94, v9, s[46:47]
	ds_bpermute_b32 v94, v187, v95
	s_lshl_b64 s[26:27], s[26:27], 9
	s_ashr_i32 s29, s28, 31
	v_readlane_b32 s30, v96, 10
	global_load_dwordx2 v[34:35], v[34:35], off
	s_waitcnt lgkmcnt(0)
	v_add_f32_e32 v9, v9, v94
	ds_bpermute_b32 v94, v188, v9
	v_lshl_add_u64 v[36:37], v[16:17], 0, s[26:27]
	s_lshl_b64 s[28:29], s[28:29], 9
	s_ashr_i32 s31, s30, 31
	v_readlane_b32 s34, v96, 11
	s_waitcnt lgkmcnt(0)
	v_add_f32_e32 v9, v9, v94
	ds_bpermute_b32 v94, v189, v9
	global_load_dwordx2 v[36:37], v[36:37], off
	v_lshl_add_u64 v[38:39], v[16:17], 0, s[28:29]
	s_lshl_b64 s[30:31], s[30:31], 9
	s_ashr_i32 s35, s34, 31
	s_waitcnt lgkmcnt(0)
	v_add_f32_e32 v9, v9, v94
	v_add_f32_e32 v9, v14, v9
	v_mul_f32_e32 v7, v7, v9
	v_mul_f32_e32 v9, 0x3d372713, v7
	v_mul_f32_e32 v9, v7, v9
	v_fma_f32 v9, v7, v9, v7
	v_mul_f32_e32 v9, 0x3fcc422a, v9
	v_mul_f32_e32 v9, 0xbfb8aa3b, v9
	v_exp_f32_e32 v9, v9
	v_lshlrev_b32_e32 v94, 4, v92
	v_readlane_b32 s38, v96, 12
	global_load_dwordx2 v[38:39], v[38:39], off
	v_add_f32_e32 v9, 1.0, v9
	v_rcp_f32_e32 v9, v9
	v_lshl_add_u64 v[40:41], v[16:17], 0, s[30:31]
	s_lshl_b64 s[34:35], s[34:35], 9
	s_ashr_i32 s39, s38, 31
	v_pk_mul_f32 v[6:7], v[6:7], v[8:9]
	v_lshrrev_b32_e32 v9, 4, v92
	v_pk_mul_f32 v[6:7], v[6:7], v[6:7] op_sel:[0,1] op_sel_hi:[1,0]
	v_cvt_f16_f32_e32 v120, v6
	v_and_b32_e32 v8, 0x7070707, v92
	v_readlane_b32 s36, v120, 0
	v_and_b32_e32 v9, 0x7070707, v9
	v_perm_b32 v8, s2, v205, v8
	v_perm_b32 v9, s2, v205, v9
	v_and_or_b32 v8, v94, s4, v8
	v_and_or_b32 v9, v92, s4, v9
	v_perm_b32 v92, v9, v8, s5
	v_perm_b32 v94, v9, v8, s33
	v_perm_b32 v95, v9, v8, s0
	v_perm_b32 v8, v9, v8, s1
	v_pk_fma_f16 v8, v8, s36, v102 op_sel_hi:[1,0,1]
	v_lshrrev_b32_e32 v102, 4, v93
	v_pk_fma_f16 v9, v92, s36, v105 op_sel_hi:[1,0,1]
	v_pk_fma_f16 v92, v94, s36, v104 op_sel_hi:[1,0,1]
	v_pk_fma_f16 v94, v95, s36, v103 op_sel_hi:[1,0,1]
	v_and_b32_e32 v95, 0x7070707, v93
	v_and_b32_e32 v102, 0x7070707, v102
	v_perm_b32 v95, s2, v205, v95
	v_perm_b32 v102, s2, v205, v102
	v_lshlrev_b32_e32 v103, 4, v93
	v_and_or_b32 v95, v103, s4, v95
	v_and_or_b32 v93, v93, s4, v102
	v_perm_b32 v102, v93, v95, s5
	v_perm_b32 v103, v93, v95, s33
	v_perm_b32 v104, v93, v95, s0
	v_perm_b32 v93, v93, v95, s1
	v_pk_fma_f16 v95, v102, s36, v101 op_sel_hi:[1,0,1]
	v_readlane_b32 s59, v120, 4
	v_lshrrev_b32_e32 v101, 4, v90
	v_pk_fma_f16 v100, v103, s36, v100 op_sel_hi:[1,0,1]
	v_pk_fma_f16 v99, v104, s36, v99 op_sel_hi:[1,0,1]
	v_pk_fma_f16 v7, v93, s36, v15 op_sel_hi:[1,0,1]
	v_and_b32_e32 v93, 0x7070707, v90
	v_and_b32_e32 v101, 0x7070707, v101
	v_perm_b32 v93, s2, v205, v93
	v_perm_b32 v101, s2, v205, v101
	v_lshlrev_b32_e32 v102, 4, v90
	v_and_or_b32 v93, v102, s4, v93
	v_and_or_b32 v90, v90, s4, v101
	v_perm_b32 v103, v90, v93, s0
	v_perm_b32 v101, v90, v93, s5
	v_perm_b32 v102, v90, v93, s33
	v_perm_b32 v90, v90, v93, s1
	v_pk_fma_f16 v93, v103, s59, v94 op_sel_hi:[1,0,1]
	v_lshrrev_b32_e32 v94, 4, v91
	v_pk_fma_f16 v8, v90, s59, v8 op_sel_hi:[1,0,1]
	v_and_b32_e32 v90, 0x7070707, v91
	v_and_b32_e32 v94, 0x7070707, v94
	v_pk_fma_f16 v9, v101, s59, v9 op_sel_hi:[1,0,1]
	v_perm_b32 v90, s2, v205, v90
	v_perm_b32 v94, s2, v205, v94
	v_lshlrev_b32_e32 v101, 4, v91
	v_and_or_b32 v90, v101, s4, v90
	v_and_or_b32 v91, v91, s4, v94
	v_pk_fma_f16 v92, v102, s59, v92 op_sel_hi:[1,0,1]
	v_perm_b32 v94, v91, v90, s5
	v_perm_b32 v102, v91, v90, s0
	v_perm_b32 v101, v91, v90, s33
	v_perm_b32 v90, v91, v90, s1
	v_pk_fma_f16 v91, v94, s59, v95 op_sel_hi:[1,0,1]
	v_pk_fma_f16 v95, v102, s59, v99 op_sel_hi:[1,0,1]
	v_readlane_b32 s60, v120, 8
	v_lshrrev_b32_e32 v99, 4, v88
	v_pk_fma_f16 v94, v101, s59, v100 op_sel_hi:[1,0,1]
	v_pk_fma_f16 v7, v90, s59, v7 op_sel_hi:[1,0,1]
	v_and_b32_e32 v90, 0x7070707, v88
	v_and_b32_e32 v99, 0x7070707, v99
	v_perm_b32 v90, s2, v205, v90
	v_perm_b32 v99, s2, v205, v99
	v_lshlrev_b32_e32 v100, 4, v88
	v_and_or_b32 v90, v100, s4, v90
	v_and_or_b32 v88, v88, s4, v99
	v_perm_b32 v100, v88, v90, s33
	v_perm_b32 v101, v88, v90, s0
	v_perm_b32 v99, v88, v90, s5
	v_perm_b32 v88, v88, v90, s1
	v_pk_fma_f16 v90, v100, s60, v92 op_sel_hi:[1,0,1]
	v_pk_fma_f16 v92, v101, s60, v93 op_sel_hi:[1,0,1]
	v_lshrrev_b32_e32 v93, 4, v89
	v_pk_fma_f16 v8, v88, s60, v8 op_sel_hi:[1,0,1]
	v_and_b32_e32 v88, 0x7070707, v89
	v_and_b32_e32 v93, 0x7070707, v93
	v_pk_fma_f16 v9, v99, s60, v9 op_sel_hi:[1,0,1]
	v_perm_b32 v88, s2, v205, v88
	v_perm_b32 v93, s2, v205, v93
	v_lshlrev_b32_e32 v99, 4, v89
	v_and_or_b32 v88, v99, s4, v88
	v_and_or_b32 v89, v89, s4, v93
	v_perm_b32 v93, v89, v88, s5
	v_perm_b32 v99, v89, v88, s33
	v_perm_b32 v100, v89, v88, s0
	v_perm_b32 v88, v89, v88, s1
	v_pk_fma_f16 v89, v93, s60, v91 op_sel_hi:[1,0,1]
	v_pk_fma_f16 v91, v99, s60, v94 op_sel_hi:[1,0,1]
	v_readlane_b32 s36, v120, 12
	v_lshrrev_b32_e32 v94, 4, v86
	v_pk_fma_f16 v93, v100, s60, v95 op_sel_hi:[1,0,1]
	v_pk_fma_f16 v7, v88, s60, v7 op_sel_hi:[1,0,1]
	v_and_b32_e32 v88, 0x7070707, v86
	v_and_b32_e32 v94, 0x7070707, v94
	v_perm_b32 v88, s2, v205, v88
	v_perm_b32 v94, s2, v205, v94
	v_lshlrev_b32_e32 v95, 4, v86
	v_and_or_b32 v88, v95, s4, v88
	v_and_or_b32 v86, v86, s4, v94
	v_perm_b32 v95, v86, v88, s33
	v_perm_b32 v99, v86, v88, s0
	v_perm_b32 v94, v86, v88, s5
	v_perm_b32 v86, v86, v88, s1
	v_pk_fma_f16 v88, v95, s36, v90 op_sel_hi:[1,0,1]
	v_pk_fma_f16 v90, v99, s36, v92 op_sel_hi:[1,0,1]
	v_lshrrev_b32_e32 v92, 4, v87
	v_pk_fma_f16 v8, v86, s36, v8 op_sel_hi:[1,0,1]
	v_and_b32_e32 v86, 0x7070707, v87
	v_and_b32_e32 v92, 0x7070707, v92
	v_pk_fma_f16 v9, v94, s36, v9 op_sel_hi:[1,0,1]
	v_perm_b32 v86, s2, v205, v86
	v_perm_b32 v92, s2, v205, v92
	v_lshlrev_b32_e32 v94, 4, v87
	v_and_or_b32 v86, v94, s4, v86
	v_and_or_b32 v87, v87, s4, v92
	v_perm_b32 v92, v87, v86, s5
	v_perm_b32 v94, v87, v86, s33
	v_perm_b32 v95, v87, v86, s0
	v_perm_b32 v86, v87, v86, s1
	v_pk_fma_f16 v87, v92, s36, v89 op_sel_hi:[1,0,1]
	v_readlane_b32 s59, v120, 16
	v_lshrrev_b32_e32 v92, 4, v84
	v_pk_fma_f16 v89, v94, s36, v91 op_sel_hi:[1,0,1]
	v_pk_fma_f16 v91, v95, s36, v93 op_sel_hi:[1,0,1]
	v_pk_fma_f16 v7, v86, s36, v7 op_sel_hi:[1,0,1]
	v_and_b32_e32 v86, 0x7070707, v84
	v_and_b32_e32 v92, 0x7070707, v92
	v_perm_b32 v86, s2, v205, v86
	v_perm_b32 v92, s2, v205, v92
	v_lshlrev_b32_e32 v93, 4, v84
	v_and_or_b32 v86, v93, s4, v86
	v_and_or_b32 v84, v84, s4, v92
	v_perm_b32 v93, v84, v86, s33
	v_perm_b32 v94, v84, v86, s0
	v_perm_b32 v92, v84, v86, s5
	v_perm_b32 v84, v84, v86, s1
	v_pk_fma_f16 v86, v93, s59, v88 op_sel_hi:[1,0,1]
	v_pk_fma_f16 v88, v94, s59, v90 op_sel_hi:[1,0,1]
	v_lshrrev_b32_e32 v90, 4, v85
	v_pk_fma_f16 v8, v84, s59, v8 op_sel_hi:[1,0,1]
	v_and_b32_e32 v84, 0x7070707, v85
	v_and_b32_e32 v90, 0x7070707, v90
	v_pk_fma_f16 v9, v92, s59, v9 op_sel_hi:[1,0,1]
	v_perm_b32 v84, s2, v205, v84
	v_perm_b32 v90, s2, v205, v90
	v_lshlrev_b32_e32 v92, 4, v85
	v_and_or_b32 v84, v92, s4, v84
	v_and_or_b32 v85, v85, s4, v90
	v_perm_b32 v90, v85, v84, s5
	v_perm_b32 v92, v85, v84, s33
	v_perm_b32 v93, v85, v84, s0
	v_perm_b32 v84, v85, v84, s1
	v_pk_fma_f16 v85, v90, s59, v87 op_sel_hi:[1,0,1]
	v_readlane_b32 s60, v120, 20
	v_lshrrev_b32_e32 v90, 4, v82
	v_pk_fma_f16 v87, v92, s59, v89 op_sel_hi:[1,0,1]
	v_pk_fma_f16 v89, v93, s59, v91 op_sel_hi:[1,0,1]
	v_pk_fma_f16 v7, v84, s59, v7 op_sel_hi:[1,0,1]
	v_and_b32_e32 v84, 0x7070707, v82
	v_and_b32_e32 v90, 0x7070707, v90
	v_perm_b32 v84, s2, v205, v84
	v_perm_b32 v90, s2, v205, v90
	v_lshlrev_b32_e32 v91, 4, v82
	v_and_or_b32 v84, v91, s4, v84
	v_and_or_b32 v82, v82, s4, v90
	v_perm_b32 v91, v82, v84, s33
	v_perm_b32 v92, v82, v84, s0
	v_perm_b32 v90, v82, v84, s5
	v_perm_b32 v82, v82, v84, s1
	v_pk_fma_f16 v84, v91, s60, v86 op_sel_hi:[1,0,1]
	v_pk_fma_f16 v86, v92, s60, v88 op_sel_hi:[1,0,1]
	v_lshrrev_b32_e32 v88, 4, v83
	v_pk_fma_f16 v8, v82, s60, v8 op_sel_hi:[1,0,1]
	v_and_b32_e32 v82, 0x7070707, v83
	v_and_b32_e32 v88, 0x7070707, v88
	v_pk_fma_f16 v9, v90, s60, v9 op_sel_hi:[1,0,1]
	v_perm_b32 v82, s2, v205, v82
	v_perm_b32 v88, s2, v205, v88
	v_lshlrev_b32_e32 v90, 4, v83
	v_and_or_b32 v82, v90, s4, v82
	v_and_or_b32 v83, v83, s4, v88
	v_perm_b32 v88, v83, v82, s5
	v_perm_b32 v90, v83, v82, s33
	v_perm_b32 v91, v83, v82, s0
	v_perm_b32 v82, v83, v82, s1
	v_pk_fma_f16 v83, v88, s60, v85 op_sel_hi:[1,0,1]
	v_readlane_b32 s36, v120, 24
	v_lshrrev_b32_e32 v88, 4, v80
	v_pk_fma_f16 v85, v90, s60, v87 op_sel_hi:[1,0,1]
	v_pk_fma_f16 v87, v91, s60, v89 op_sel_hi:[1,0,1]
	v_pk_fma_f16 v7, v82, s60, v7 op_sel_hi:[1,0,1]
	v_and_b32_e32 v82, 0x7070707, v80
	v_and_b32_e32 v88, 0x7070707, v88
	v_perm_b32 v82, s2, v205, v82
	v_perm_b32 v88, s2, v205, v88
	v_lshlrev_b32_e32 v89, 4, v80
	v_and_or_b32 v82, v89, s4, v82
	v_and_or_b32 v80, v80, s4, v88
	v_perm_b32 v89, v80, v82, s33
	v_perm_b32 v90, v80, v82, s0
	v_perm_b32 v88, v80, v82, s5
	v_perm_b32 v80, v80, v82, s1
	v_pk_fma_f16 v82, v89, s36, v84 op_sel_hi:[1,0,1]
	v_pk_fma_f16 v84, v90, s36, v86 op_sel_hi:[1,0,1]
	v_lshrrev_b32_e32 v86, 4, v81
	v_pk_fma_f16 v8, v80, s36, v8 op_sel_hi:[1,0,1]
	v_and_b32_e32 v80, 0x7070707, v81
	v_and_b32_e32 v86, 0x7070707, v86
	v_pk_fma_f16 v9, v88, s36, v9 op_sel_hi:[1,0,1]
	v_perm_b32 v80, s2, v205, v80
	v_perm_b32 v86, s2, v205, v86
	v_lshlrev_b32_e32 v88, 4, v81
	v_and_or_b32 v80, v88, s4, v80
	v_and_or_b32 v81, v81, s4, v86
	v_perm_b32 v86, v81, v80, s5
	v_perm_b32 v88, v81, v80, s33
	v_perm_b32 v89, v81, v80, s0
	v_perm_b32 v80, v81, v80, s1
	v_pk_fma_f16 v81, v86, s36, v83 op_sel_hi:[1,0,1]
	v_readlane_b32 s59, v120, 28
	v_lshrrev_b32_e32 v86, 4, v78
	v_pk_fma_f16 v83, v88, s36, v85 op_sel_hi:[1,0,1]
	v_pk_fma_f16 v85, v89, s36, v87 op_sel_hi:[1,0,1]
	v_pk_fma_f16 v7, v80, s36, v7 op_sel_hi:[1,0,1]
	v_and_b32_e32 v80, 0x7070707, v78
	v_and_b32_e32 v86, 0x7070707, v86
	v_perm_b32 v80, s2, v205, v80
	v_perm_b32 v86, s2, v205, v86
	v_lshlrev_b32_e32 v87, 4, v78
	v_and_or_b32 v80, v87, s4, v80
	v_and_or_b32 v78, v78, s4, v86
	v_perm_b32 v87, v78, v80, s33
	v_perm_b32 v88, v78, v80, s0
	v_perm_b32 v86, v78, v80, s5
	v_perm_b32 v78, v78, v80, s1
	v_pk_fma_f16 v80, v87, s59, v82 op_sel_hi:[1,0,1]
	v_pk_fma_f16 v82, v88, s59, v84 op_sel_hi:[1,0,1]
	v_lshrrev_b32_e32 v84, 4, v79
	v_pk_fma_f16 v8, v78, s59, v8 op_sel_hi:[1,0,1]
	v_and_b32_e32 v78, 0x7070707, v79
	v_and_b32_e32 v84, 0x7070707, v84
	v_pk_fma_f16 v9, v86, s59, v9 op_sel_hi:[1,0,1]
	v_perm_b32 v78, s2, v205, v78
	v_perm_b32 v84, s2, v205, v84
	v_lshlrev_b32_e32 v86, 4, v79
	v_and_or_b32 v78, v86, s4, v78
	v_and_or_b32 v79, v79, s4, v84
	v_perm_b32 v84, v79, v78, s5
	v_perm_b32 v86, v79, v78, s33
	v_perm_b32 v87, v79, v78, s0
	v_perm_b32 v78, v79, v78, s1
	v_pk_fma_f16 v79, v84, s59, v81 op_sel_hi:[1,0,1]
	v_readlane_b32 s60, v120, 32
	v_lshrrev_b32_e32 v84, 4, v76
	v_pk_fma_f16 v81, v86, s59, v83 op_sel_hi:[1,0,1]
	v_pk_fma_f16 v83, v87, s59, v85 op_sel_hi:[1,0,1]
	v_pk_fma_f16 v7, v78, s59, v7 op_sel_hi:[1,0,1]
	v_and_b32_e32 v78, 0x7070707, v76
	v_and_b32_e32 v84, 0x7070707, v84
	v_perm_b32 v78, s2, v205, v78
	v_perm_b32 v84, s2, v205, v84
	v_lshlrev_b32_e32 v85, 4, v76
	v_and_or_b32 v78, v85, s4, v78
	v_and_or_b32 v76, v76, s4, v84
	v_perm_b32 v85, v76, v78, s33
	v_perm_b32 v86, v76, v78, s0
	v_perm_b32 v84, v76, v78, s5
	v_perm_b32 v76, v76, v78, s1
	v_pk_fma_f16 v78, v85, s60, v80 op_sel_hi:[1,0,1]
	v_pk_fma_f16 v80, v86, s60, v82 op_sel_hi:[1,0,1]
	v_lshrrev_b32_e32 v82, 4, v77
	v_pk_fma_f16 v8, v76, s60, v8 op_sel_hi:[1,0,1]
	v_and_b32_e32 v76, 0x7070707, v77
	v_and_b32_e32 v82, 0x7070707, v82
	v_pk_fma_f16 v9, v84, s60, v9 op_sel_hi:[1,0,1]
	v_perm_b32 v76, s2, v205, v76
	v_perm_b32 v82, s2, v205, v82
	v_lshlrev_b32_e32 v84, 4, v77
	v_and_or_b32 v76, v84, s4, v76
	v_and_or_b32 v77, v77, s4, v82
	v_perm_b32 v82, v77, v76, s5
	v_perm_b32 v84, v77, v76, s33
	v_perm_b32 v85, v77, v76, s0
	v_perm_b32 v76, v77, v76, s1
	v_pk_fma_f16 v77, v82, s60, v79 op_sel_hi:[1,0,1]
	v_readlane_b32 s36, v120, 36
	v_lshrrev_b32_e32 v82, 4, v70
	v_pk_fma_f16 v79, v84, s60, v81 op_sel_hi:[1,0,1]
	v_pk_fma_f16 v81, v85, s60, v83 op_sel_hi:[1,0,1]
	v_pk_fma_f16 v7, v76, s60, v7 op_sel_hi:[1,0,1]
	v_and_b32_e32 v76, 0x7070707, v70
	v_and_b32_e32 v82, 0x7070707, v82
	v_perm_b32 v76, s2, v205, v76
	v_perm_b32 v82, s2, v205, v82
	v_lshlrev_b32_e32 v83, 4, v70
	v_and_or_b32 v76, v83, s4, v76
	v_and_or_b32 v70, v70, s4, v82
	v_perm_b32 v83, v70, v76, s33
	v_perm_b32 v84, v70, v76, s0
	v_perm_b32 v82, v70, v76, s5
	v_perm_b32 v70, v70, v76, s1
	v_pk_fma_f16 v76, v83, s36, v78 op_sel_hi:[1,0,1]
	v_pk_fma_f16 v78, v84, s36, v80 op_sel_hi:[1,0,1]
	v_lshrrev_b32_e32 v80, 4, v71
	v_pk_fma_f16 v8, v70, s36, v8 op_sel_hi:[1,0,1]
	v_and_b32_e32 v70, 0x7070707, v71
	v_and_b32_e32 v80, 0x7070707, v80
	v_pk_fma_f16 v9, v82, s36, v9 op_sel_hi:[1,0,1]
	v_perm_b32 v70, s2, v205, v70
	v_perm_b32 v80, s2, v205, v80
	v_lshlrev_b32_e32 v82, 4, v71
	v_and_or_b32 v70, v82, s4, v70
	v_and_or_b32 v71, v71, s4, v80
	v_perm_b32 v80, v71, v70, s5
	v_perm_b32 v82, v71, v70, s33
	v_perm_b32 v83, v71, v70, s0
	v_perm_b32 v70, v71, v70, s1
	v_pk_fma_f16 v71, v80, s36, v77 op_sel_hi:[1,0,1]
	v_readlane_b32 s59, v120, 40
	v_lshrrev_b32_e32 v80, 4, v66
	v_pk_fma_f16 v77, v82, s36, v79 op_sel_hi:[1,0,1]
	v_pk_fma_f16 v79, v83, s36, v81 op_sel_hi:[1,0,1]
	v_pk_fma_f16 v7, v70, s36, v7 op_sel_hi:[1,0,1]
	v_and_b32_e32 v70, 0x7070707, v66
	v_and_b32_e32 v80, 0x7070707, v80
	v_perm_b32 v70, s2, v205, v70
	v_perm_b32 v80, s2, v205, v80
	v_lshlrev_b32_e32 v81, 4, v66
	v_and_or_b32 v70, v81, s4, v70
	v_and_or_b32 v66, v66, s4, v80
	v_perm_b32 v81, v66, v70, s33
	v_perm_b32 v82, v66, v70, s0
	v_perm_b32 v80, v66, v70, s5
	v_perm_b32 v66, v66, v70, s1
	v_pk_fma_f16 v70, v81, s59, v76 op_sel_hi:[1,0,1]
	v_pk_fma_f16 v76, v82, s59, v78 op_sel_hi:[1,0,1]
	v_lshrrev_b32_e32 v78, 4, v67
	v_pk_fma_f16 v8, v66, s59, v8 op_sel_hi:[1,0,1]
	v_and_b32_e32 v66, 0x7070707, v67
	v_and_b32_e32 v78, 0x7070707, v78
	v_pk_fma_f16 v9, v80, s59, v9 op_sel_hi:[1,0,1]
	v_perm_b32 v66, s2, v205, v66
	v_perm_b32 v78, s2, v205, v78
	v_lshlrev_b32_e32 v80, 4, v67
	v_and_or_b32 v66, v80, s4, v66
	v_and_or_b32 v67, v67, s4, v78
	v_perm_b32 v78, v67, v66, s5
	v_perm_b32 v80, v67, v66, s33
	v_perm_b32 v81, v67, v66, s0
	v_perm_b32 v66, v67, v66, s1
	v_pk_fma_f16 v67, v78, s59, v71 op_sel_hi:[1,0,1]
	v_readlane_b32 s60, v120, 44
	v_lshrrev_b32_e32 v78, 4, v72
	v_pk_fma_f16 v71, v80, s59, v77 op_sel_hi:[1,0,1]
	v_pk_fma_f16 v77, v81, s59, v79 op_sel_hi:[1,0,1]
	v_pk_fma_f16 v7, v66, s59, v7 op_sel_hi:[1,0,1]
	v_and_b32_e32 v66, 0x7070707, v72
	v_and_b32_e32 v78, 0x7070707, v78
	v_perm_b32 v66, s2, v205, v66
	v_perm_b32 v78, s2, v205, v78
	v_lshlrev_b32_e32 v79, 4, v72
	v_and_or_b32 v66, v79, s4, v66
	v_and_or_b32 v72, v72, s4, v78
	v_perm_b32 v80, v72, v66, s0
	v_perm_b32 v78, v72, v66, s5
	v_perm_b32 v79, v72, v66, s33
	v_perm_b32 v66, v72, v66, s1
	v_pk_fma_f16 v72, v80, s60, v76 op_sel_hi:[1,0,1]
	v_lshrrev_b32_e32 v76, 4, v73
	v_pk_fma_f16 v8, v66, s60, v8 op_sel_hi:[1,0,1]
	v_and_b32_e32 v66, 0x7070707, v73
	v_and_b32_e32 v76, 0x7070707, v76
	v_pk_fma_f16 v9, v78, s60, v9 op_sel_hi:[1,0,1]
	v_perm_b32 v66, s2, v205, v66
	v_perm_b32 v76, s2, v205, v76
	v_lshlrev_b32_e32 v78, 4, v73
	v_and_or_b32 v66, v78, s4, v66
	v_and_or_b32 v73, v73, s4, v76
	v_perm_b32 v76, v73, v66, s5
	v_pk_fma_f16 v70, v79, s60, v70 op_sel_hi:[1,0,1]
	v_perm_b32 v78, v73, v66, s33
	v_perm_b32 v79, v73, v66, s0
	v_perm_b32 v66, v73, v66, s1
	v_pk_fma_f16 v67, v76, s60, v67 op_sel_hi:[1,0,1]
	v_readlane_b32 s36, v120, 48
	v_lshrrev_b32_e32 v76, 4, v68
	v_pk_fma_f16 v71, v78, s60, v71 op_sel_hi:[1,0,1]
	v_pk_fma_f16 v73, v79, s60, v77 op_sel_hi:[1,0,1]
	v_pk_fma_f16 v7, v66, s60, v7 op_sel_hi:[1,0,1]
	v_and_b32_e32 v66, 0x7070707, v68
	v_and_b32_e32 v76, 0x7070707, v76
	v_perm_b32 v66, s2, v205, v66
	v_perm_b32 v76, s2, v205, v76
	v_lshlrev_b32_e32 v77, 4, v68
	v_and_or_b32 v66, v77, s4, v66
	v_and_or_b32 v68, v68, s4, v76
	v_perm_b32 v77, v68, v66, s33
	v_perm_b32 v78, v68, v66, s0
	v_perm_b32 v76, v68, v66, s5
	v_perm_b32 v66, v68, v66, s1
	v_pk_fma_f16 v68, v77, s36, v70 op_sel_hi:[1,0,1]
	v_pk_fma_f16 v70, v78, s36, v72 op_sel_hi:[1,0,1]
	v_lshrrev_b32_e32 v72, 4, v69
	v_pk_fma_f16 v8, v66, s36, v8 op_sel_hi:[1,0,1]
	v_and_b32_e32 v66, 0x7070707, v69
	v_and_b32_e32 v72, 0x7070707, v72
	v_pk_fma_f16 v9, v76, s36, v9 op_sel_hi:[1,0,1]
	v_perm_b32 v66, s2, v205, v66
	v_perm_b32 v72, s2, v205, v72
	v_lshlrev_b32_e32 v76, 4, v69
	v_and_or_b32 v66, v76, s4, v66
	v_and_or_b32 v69, v69, s4, v72
	v_perm_b32 v72, v69, v66, s5
	v_perm_b32 v76, v69, v66, s33
	v_perm_b32 v77, v69, v66, s0
	v_perm_b32 v66, v69, v66, s1
	v_pk_fma_f16 v67, v72, s36, v67 op_sel_hi:[1,0,1]
	v_readlane_b32 s59, v120, 52
	v_lshrrev_b32_e32 v72, 4, v64
	v_pk_fma_f16 v69, v76, s36, v71 op_sel_hi:[1,0,1]
	v_pk_fma_f16 v71, v77, s36, v73 op_sel_hi:[1,0,1]
	v_pk_fma_f16 v7, v66, s36, v7 op_sel_hi:[1,0,1]
	v_and_b32_e32 v66, 0x7070707, v64
	v_and_b32_e32 v72, 0x7070707, v72
	v_perm_b32 v66, s2, v205, v66
	v_perm_b32 v72, s2, v205, v72
	v_lshlrev_b32_e32 v73, 4, v64
	v_and_or_b32 v66, v73, s4, v66
	v_and_or_b32 v64, v64, s4, v72
	v_perm_b32 v73, v64, v66, s33
	v_perm_b32 v76, v64, v66, s0
	v_perm_b32 v72, v64, v66, s5
	v_perm_b32 v64, v64, v66, s1
	v_pk_fma_f16 v66, v73, s59, v68 op_sel_hi:[1,0,1]
	v_pk_fma_f16 v68, v76, s59, v70 op_sel_hi:[1,0,1]
	v_lshrrev_b32_e32 v70, 4, v65
	v_pk_fma_f16 v8, v64, s59, v8 op_sel_hi:[1,0,1]
	v_and_b32_e32 v64, 0x7070707, v65
	v_and_b32_e32 v70, 0x7070707, v70
	v_pk_fma_f16 v9, v72, s59, v9 op_sel_hi:[1,0,1]
	v_perm_b32 v64, s2, v205, v64
	v_perm_b32 v70, s2, v205, v70
	v_lshlrev_b32_e32 v72, 4, v65
	v_and_or_b32 v64, v72, s4, v64
	v_and_or_b32 v65, v65, s4, v70
	v_perm_b32 v70, v65, v64, s5
	v_perm_b32 v72, v65, v64, s33
	v_perm_b32 v73, v65, v64, s0
	v_perm_b32 v64, v65, v64, s1
	v_pk_fma_f16 v65, v70, s59, v67 op_sel_hi:[1,0,1]
	v_readlane_b32 s60, v120, 56
	v_lshrrev_b32_e32 v70, 4, v62
	v_pk_fma_f16 v67, v72, s59, v69 op_sel_hi:[1,0,1]
	v_pk_fma_f16 v69, v73, s59, v71 op_sel_hi:[1,0,1]
	v_pk_fma_f16 v7, v64, s59, v7 op_sel_hi:[1,0,1]
	v_and_b32_e32 v64, 0x7070707, v62
	v_and_b32_e32 v70, 0x7070707, v70
	v_perm_b32 v64, s2, v205, v64
	v_perm_b32 v70, s2, v205, v70
	v_lshlrev_b32_e32 v71, 4, v62
	v_and_or_b32 v64, v71, s4, v64
	v_and_or_b32 v62, v62, s4, v70
	v_perm_b32 v71, v62, v64, s33
	v_perm_b32 v72, v62, v64, s0
	v_perm_b32 v70, v62, v64, s5
	v_perm_b32 v62, v62, v64, s1
	v_pk_fma_f16 v64, v71, s60, v66 op_sel_hi:[1,0,1]
	v_pk_fma_f16 v66, v72, s60, v68 op_sel_hi:[1,0,1]
	v_lshrrev_b32_e32 v68, 4, v63
	v_pk_fma_f16 v8, v62, s60, v8 op_sel_hi:[1,0,1]
	v_and_b32_e32 v62, 0x7070707, v63
	v_and_b32_e32 v68, 0x7070707, v68
	v_pk_fma_f16 v9, v70, s60, v9 op_sel_hi:[1,0,1]
	v_perm_b32 v62, s2, v205, v62
	v_perm_b32 v68, s2, v205, v68
	v_lshlrev_b32_e32 v70, 4, v63
	v_and_or_b32 v62, v70, s4, v62
	v_and_or_b32 v63, v63, s4, v68
	v_perm_b32 v68, v63, v62, s5
	v_perm_b32 v70, v63, v62, s33
	v_perm_b32 v71, v63, v62, s0
	v_perm_b32 v62, v63, v62, s1
	v_pk_fma_f16 v7, v62, s60, v7 op_sel_hi:[1,0,1]
	v_readlane_b32 s36, v120, 60
	v_lshrrev_b32_e32 v62, 4, v50
	v_pk_fma_f16 v63, v68, s60, v65 op_sel_hi:[1,0,1]
	v_pk_fma_f16 v65, v70, s60, v67 op_sel_hi:[1,0,1]
	v_pk_fma_f16 v67, v71, s60, v69 op_sel_hi:[1,0,1]
	v_and_b32_e32 v15, 0x7070707, v50
	v_and_b32_e32 v62, 0x7070707, v62
	v_perm_b32 v15, s2, v205, v15
	v_perm_b32 v62, s2, v205, v62
	v_lshlrev_b32_e32 v68, 4, v50
	v_and_or_b32 v15, v68, s4, v15
	v_and_or_b32 v50, v50, s4, v62
	v_perm_b32 v62, v50, v15, s5
	v_perm_b32 v68, v50, v15, s33
	v_perm_b32 v69, v50, v15, s0
	v_perm_b32 v15, v50, v15, s1
	v_pk_fma_f16 v105, v62, s36, v9 op_sel_hi:[1,0,1]
	v_lshrrev_b32_e32 v9, 4, v51
	v_pk_fma_f16 v102, v15, s36, v8 op_sel_hi:[1,0,1]
	v_and_b32_e32 v8, 0x7070707, v51
	v_and_b32_e32 v9, 0x7070707, v9
	v_perm_b32 v8, s2, v205, v8
	v_perm_b32 v9, s2, v205, v9
	v_lshlrev_b32_e32 v15, 4, v51
	v_and_or_b32 v8, v15, s4, v8
	v_and_or_b32 v9, v51, s4, v9
	v_perm_b32 v15, v9, v8, s5
	v_perm_b32 v50, v9, v8, s33
	v_perm_b32 v51, v9, v8, s0
	v_perm_b32 v8, v9, v8, s1
	v_pk_fma_f16 v104, v68, s36, v64 op_sel_hi:[1,0,1]
	v_pk_fma_f16 v103, v69, s36, v66 op_sel_hi:[1,0,1]
	v_pk_fma_f16 v101, v15, s36, v63 op_sel_hi:[1,0,1]
	v_pk_fma_f16 v100, v50, s36, v65 op_sel_hi:[1,0,1]
	v_pk_fma_f16 v99, v51, s36, v67 op_sel_hi:[1,0,1]
	v_pk_fma_f16 v15, v8, s36, v7 op_sel_hi:[1,0,1]
	v_lshl_add_u64 v[6:7], v[18:19], 0, s[10:11]
	global_load_dwordx2 v[92:93], v[6:7], off
	v_lshl_add_u64 v[6:7], v[18:19], 0, s[12:13]
	global_load_dwordx2 v[90:91], v[6:7], off
	v_lshl_add_u64 v[6:7], v[18:19], 0, s[14:15]
	global_load_dwordx2 v[88:89], v[6:7], off
	v_lshl_add_u64 v[6:7], v[18:19], 0, s[16:17]
	global_load_dwordx2 v[86:87], v[6:7], off
	v_lshl_add_u64 v[6:7], v[18:19], 0, s[18:19]
	global_load_dwordx2 v[84:85], v[6:7], off
	v_lshl_add_u64 v[6:7], v[18:19], 0, s[20:21]
	global_load_dwordx2 v[82:83], v[6:7], off
	v_lshl_add_u64 v[6:7], v[18:19], 0, s[22:23]
	global_load_dwordx2 v[80:81], v[6:7], off
	v_lshl_add_u64 v[6:7], v[18:19], 0, s[24:25]
	global_load_dwordx2 v[78:79], v[6:7], off
	v_lshl_add_u64 v[6:7], v[18:19], 0, s[26:27]
	global_load_dwordx2 v[76:77], v[6:7], off
	v_lshl_add_u64 v[6:7], v[18:19], 0, s[28:29]
	v_readlane_b32 s50, v96, 13
	global_load_dwordx2 v[70:71], v[6:7], off
	v_lshl_add_u64 v[6:7], v[18:19], 0, s[30:31]
	global_load_dwordx2 v[40:41], v[40:41], off
	v_lshl_add_u64 v[52:53], v[16:17], 0, s[34:35]
	s_lshl_b64 s[38:39], s[38:39], 9
	s_ashr_i32 s51, s50, 31
	v_readlane_b32 s52, v96, 14
	global_load_dwordx2 v[66:67], v[6:7], off
	v_lshl_add_u64 v[6:7], v[18:19], 0, s[34:35]
	global_load_dwordx2 v[60:61], v[52:53], off
	global_load_dwordx2 v[72:73], v[6:7], off
	v_lshl_add_u64 v[52:53], v[16:17], 0, s[38:39]
	s_lshl_b64 s[50:51], s[50:51], 9
	s_ashr_i32 s53, s52, 31
	v_readlane_b32 s54, v96, 15
	v_lshl_add_u64 v[6:7], v[18:19], 0, s[38:39]
	global_load_dwordx2 v[58:59], v[52:53], off
	global_load_dwordx2 v[68:69], v[6:7], off
	v_lshl_add_u64 v[52:53], v[16:17], 0, s[50:51]
	s_lshl_b64 s[52:53], s[52:53], 9
	s_ashr_i32 s55, s54, 31
	v_lshl_add_u64 v[6:7], v[18:19], 0, s[50:51]
	global_load_dwordx2 v[56:57], v[52:53], off
	global_load_dwordx2 v[64:65], v[6:7], off
	v_lshl_add_u64 v[52:53], v[16:17], 0, s[52:53]
	s_lshl_b64 s[54:55], s[54:55], 9
	v_lshl_add_u64 v[6:7], v[18:19], 0, s[52:53]
	global_load_dwordx2 v[54:55], v[52:53], off
	global_load_dwordx2 v[62:63], v[6:7], off
	v_lshl_add_u64 v[52:53], v[16:17], 0, s[54:55]
	v_lshl_add_u64 v[6:7], v[18:19], 0, s[54:55]
	global_load_dwordx2 v[52:53], v[52:53], off
	s_cmpk_eq_i32 s56, 0x90
	global_load_dwordx2 v[50:51], v[6:7], off
	s_cbranch_scc0 .LBB0_770
	v_lshl_add_u64 v[94:95], v[2:3], 2, v[44:45]
	global_load_dwordx4 v[106:109], v[94:95], off offset:48
	global_load_dwordx4 v[8:11], v[94:95], off offset:32
	global_load_dwordx4 v[4:7], v[94:95], off offset:16
	global_load_dwordx4 v[0:3], v[94:95], off
	v_cvt_f32_f16_sdwa v13, v105 dst_sel:DWORD dst_unused:UNUSED_PAD src0_sel:WORD_1
	v_cvt_f32_f16_e32 v12, v105
	s_mov_b32 s12, 0x800000
	v_readlane_b32 s10, v255, 5
	v_readlane_b32 s11, v255, 6
	s_waitcnt vmcnt(0)
	v_pk_add_f32 v[0:1], v[0:1], v[12:13]
	v_cvt_f32_f16_sdwa v13, v104 dst_sel:DWORD dst_unused:UNUSED_PAD src0_sel:WORD_1
	v_cvt_f32_f16_e32 v12, v104
	v_lshl_add_u64 v[48:49], v[48:49], 0, s[10:11]
	v_pk_add_f32 v[2:3], v[2:3], v[12:13]
	v_cvt_f32_f16_sdwa v13, v103 dst_sel:DWORD dst_unused:UNUSED_PAD src0_sel:WORD_1
	v_cvt_f32_f16_e32 v12, v103
	global_store_dwordx4 v[94:95], v[0:3], off
	v_pk_add_f32 v[4:5], v[4:5], v[12:13]
	v_cvt_f32_f16_sdwa v13, v102 dst_sel:DWORD dst_unused:UNUSED_PAD src0_sel:WORD_1
	v_cvt_f32_f16_e32 v12, v102
	v_mov_b32_e32 v102, v1
	v_mov_b32_e32 v103, v5
	v_pk_mul_f32 v[102:103], v[102:103], v[102:103]
	v_pk_add_f32 v[6:7], v[6:7], v[12:13]
	v_mov_b32_e32 v12, v0
	v_mov_b32_e32 v13, v4
	v_pk_fma_f32 v[12:13], v[12:13], v[12:13], v[102:103]
	v_mov_b32_e32 v102, v2
	v_mov_b32_e32 v103, v6
	v_pk_fma_f32 v[12:13], v[102:103], v[102:103], v[12:13]
	v_mov_b32_e32 v102, v3
	v_mov_b32_e32 v103, v7
	v_pk_fma_f32 v[102:103], v[102:103], v[102:103], v[12:13]
	v_cvt_f32_f16_sdwa v13, v101 dst_sel:DWORD dst_unused:UNUSED_PAD src0_sel:WORD_1
	v_cvt_f32_f16_e32 v12, v101
	v_cvt_f32_f16_sdwa v101, v15 dst_sel:DWORD dst_unused:UNUSED_PAD src0_sel:WORD_1
	global_store_dwordx4 v[94:95], v[4:7], off offset:16
	v_pk_add_f32 v[8:9], v[8:9], v[12:13]
	v_cvt_f32_f16_sdwa v13, v100 dst_sel:DWORD dst_unused:UNUSED_PAD src0_sel:WORD_1
	v_cvt_f32_f16_e32 v12, v100
	v_cvt_f32_f16_e32 v100, v15
	v_pk_add_f32 v[10:11], v[10:11], v[12:13]
	v_cvt_f32_f16_sdwa v13, v99 dst_sel:DWORD dst_unused:UNUSED_PAD src0_sel:WORD_1
	v_cvt_f32_f16_e32 v12, v99
	v_pk_add_f32 v[14:15], v[108:109], v[100:101]
	v_mov_b32_e32 v100, v9
	global_store_dwordx4 v[94:95], v[8:11], off offset:32
	v_pk_add_f32 v[12:13], v[106:107], v[12:13]
	global_store_dwordx4 v[94:95], v[12:15], off offset:48
	v_mov_b32_e32 v101, v13
	v_mov_b32_e32 v94, v8
	v_mov_b32_e32 v95, v12
	v_pk_mul_f32 v[100:101], v[100:101], v[100:101]
	v_add_f32_e32 v99, v102, v103
	v_pk_fma_f32 v[94:95], v[94:95], v[94:95], v[100:101]
	v_mov_b32_e32 v100, v10
	v_mov_b32_e32 v101, v14
	v_pk_fma_f32 v[94:95], v[100:101], v[100:101], v[94:95]
	v_mov_b32_e32 v100, v11
	v_mov_b32_e32 v101, v15
	v_pk_fma_f32 v[94:95], v[100:101], v[100:101], v[94:95]
	global_load_dwordx4 v[100:103], v[46:47], off offset:48
	global_load_dwordx4 v[104:107], v[46:47], off offset:32
	global_load_dwordx4 v[108:111], v[46:47], off offset:16
	global_load_dwordx4 v[112:115], v[46:47], off
	v_add_f32_e32 v94, v99, v94
	v_add_f32_e32 v94, v94, v95
	ds_bpermute_b32 v95, v184, v94
	s_waitcnt lgkmcnt(0)
	v_add_f32_e32 v94, v94, v95
	ds_bpermute_b32 v95, v185, v94
	s_waitcnt lgkmcnt(0)
	v_add_f32_e32 v94, v94, v95
	ds_bpermute_b32 v95, v186, v94
	s_waitcnt lgkmcnt(0)
	v_add_f32_e32 v94, v94, v95
	ds_bpermute_b32 v95, v187, v94
	s_waitcnt lgkmcnt(0)
	v_add_f32_e32 v94, v94, v95
	ds_bpermute_b32 v95, v188, v94
	s_waitcnt lgkmcnt(0)
	v_add_f32_e32 v94, v94, v95
	ds_bpermute_b32 v95, v189, v94
	s_waitcnt lgkmcnt(0)
	v_add_f32_e32 v94, v94, v95
	v_fmamk_f32 v94, v94, 0x3a800000, v191
	v_cmp_gt_f32_e32 vcc, s12, v94
	v_mul_f32_e32 v95, 0x4b800000, v94
	s_nop 0
	v_cndmask_b32_e32 v94, v94, v95, vcc
	v_rsq_f32_e32 v94, v94
	s_nop 0
	v_mul_f32_e32 v95, 0x45800000, v94
	v_cndmask_b32_e32 v94, v94, v95, vcc
	v_pk_mul_f32 v[0:1], v[0:1], v[94:95] op_sel_hi:[1,0]
	v_pk_mul_f32 v[2:3], v[2:3], v[94:95] op_sel_hi:[1,0]
	s_waitcnt vmcnt(0)
	v_pk_mul_f32 v[0:1], v[112:113], v[0:1]
	v_pk_mul_f32 v[2:3], v[114:115], v[2:3]
	v_cvt_pk_bf16_f32 v0, v0, v1
	v_cvt_pk_bf16_f32 v1, v2, v3
	v_pk_mul_f32 v[2:3], v[4:5], v[94:95] op_sel_hi:[1,0]
	v_pk_mul_f32 v[4:5], v[6:7], v[94:95] op_sel_hi:[1,0]
	v_pk_mul_f32 v[2:3], v[108:109], v[2:3]
	v_pk_mul_f32 v[4:5], v[110:111], v[4:5]
	v_cvt_pk_bf16_f32 v2, v2, v3
	v_cvt_pk_bf16_f32 v3, v4, v5
	v_pk_mul_f32 v[4:5], v[8:9], v[94:95] op_sel_hi:[1,0]
	v_pk_mul_f32 v[6:7], v[10:11], v[94:95] op_sel_hi:[1,0]
	v_pk_mul_f32 v[4:5], v[104:105], v[4:5]
	v_pk_mul_f32 v[6:7], v[6:7], v[106:107]
	v_cvt_pk_bf16_f32 v4, v4, v5
	v_cvt_pk_bf16_f32 v5, v6, v7
	v_pk_mul_f32 v[6:7], v[12:13], v[94:95] op_sel_hi:[1,0]
	v_pk_mul_f32 v[8:9], v[14:15], v[94:95] op_sel_hi:[1,0]
	v_pk_mul_f32 v[6:7], v[6:7], v[100:101]
	v_pk_mul_f32 v[8:9], v[8:9], v[102:103]
	v_cvt_pk_bf16_f32 v6, v6, v7
	v_cvt_pk_bf16_f32 v7, v8, v9
	global_store_dwordx4 v[74:75], v[0:3], off
	global_store_dwordx4 v[74:75], v[4:7], off offset:16
	s_nop 0
	v_mov_b32_e32 v0, v98
	s_andn2_b64 exec, exec, s[8:9]
	s_cbranch_execnz .LBB0_769
